# deeper LDS read pipeline: router-logit ds_read_b128 chain 7 deep
# baseline (speedup 1.0000x reference)
.LBB0_2123:
	v_lshl_add_u64 v[28:29], s[44:45], 0, v[16:17]
	v_add_co_u32_e32 v4, vcc, 0x37a00000, v28
	s_add_i32 s0, s80, s8
	s_nop 0
	v_addc_co_u32_e32 v5, vcc, 0, v29, vcc
	global_load_dwordx2 v[62:63], v[4:5], off
	global_load_dwordx2 v[60:61], v[4:5], off offset:512
	global_load_dwordx2 v[48:49], v[4:5], off offset:1024
	s_waitcnt lgkmcnt(0)
	global_load_dwordx2 v[6:7], v[4:5], off offset:1536
	global_load_dwordx2 v[46:47], v[4:5], off offset:2048
	global_load_dwordx2 v[44:45], v[4:5], off offset:2560
	global_load_dwordx2 v[42:43], v[4:5], off offset:3072
	s_nop 0
	global_load_dwordx2 v[4:5], v[4:5], off offset:3584
	s_cmp_lt_i32 s0, s86
	s_cselect_b32 s48, s0, s8
	s_ashr_i32 s49, s48, 31
	s_lshl_b64 s[50:51], s[48:49], 12
	v_lshl_add_u64 v[218:219], v[8:9], 0, s[50:51]
	global_load_dwordx2 v[40:41], v[218:219], off
	global_load_dwordx2 v[38:39], v[218:219], off offset:512
	global_load_dwordx2 v[36:37], v[218:219], off offset:1024
	global_load_dwordx2 v[250:251], v[218:219], off offset:1536
	global_load_dwordx2 v[34:35], v[218:219], off offset:2048
	global_load_dwordx2 v[32:33], v[218:219], off offset:2560
	global_load_dwordx2 v[30:31], v[218:219], off offset:3072
	global_load_dwordx2 v[50:51], v[218:219], off offset:3584
	v_mov_b32_e32 v2, s81
	s_min_i32 s0, s8, 0x4000
	s_lshr_b32 s0, s0, 12
	s_mulk_i32 s0, 0x3000
	s_ashr_i32 s1, s0, 31
	s_lshl_b64 s[0:1], s[0:1], 2
	s_add_u32 s2, s6, s0
	s_addc_u32 s3, s7, s1
	s_min_i32 s0, s48, 0x4000
	s_lshr_b32 s0, s0, 12
	s_mulk_i32 s0, 0x3000
	s_ashr_i32 s1, s0, 31
	s_lshl_b64 s[0:1], s[0:1], 2
	s_add_u32 s0, s6, s0
	s_addc_u32 s1, s7, s1
	s_waitcnt vmcnt(15)
	v_and_b32_e32 v103, 0xffff0000, v63
	v_and_b32_e32 v101, 0xffff0000, v62
	v_lshlrev_b32_e32 v102, 16, v63
	s_waitcnt vmcnt(12)
	v_lshlrev_b32_e32 v25, 16, v6
	s_waitcnt vmcnt(8)
	v_lshlrev_b32_e32 v21, 16, v4
	v_and_b32_e32 v19, 0xffff0000, v4
	v_lshlrev_b32_e32 v58, 16, v5
	v_and_b32_e32 v59, 0xffff0000, v5
	v_and_b32_e32 v23, 0xffff0000, v6
	v_lshlrev_b32_e32 v26, 16, v7
	v_and_b32_e32 v27, 0xffff0000, v7
	ds_read_b64 v[64:65], v2
	v_mul_f32_e32 v2, v103, v103
	v_lshlrev_b32_e32 v100, 16, v62
	v_pk_fma_f32 v[62:63], v[102:103], v[102:103], v[2:3] op_sel_hi:[1,1,0]
	v_and_b32_e32 v99, 0xffff0000, v61
	v_and_b32_e32 v98, 0xffff0000, v60
	v_mul_f32_e32 v2, v101, v101
	v_lshlrev_b32_e32 v95, 16, v61
	v_lshlrev_b32_e32 v94, 16, v60
	v_pk_mul_f32 v[60:61], v[98:99], v[98:99]
	v_lshlrev_b32_e32 v90, 16, v48
	v_and_b32_e32 v91, 0xffff0000, v48
	v_lshlrev_b32_e32 v96, 16, v49
	v_and_b32_e32 v97, 0xffff0000, v49
	v_pk_fma_f32 v[48:49], v[100:101], v[100:101], v[2:3] op_sel_hi:[1,1,0]
	s_waitcnt lgkmcnt(0)
	v_readfirstlane_b32 s9, v64
	v_readfirstlane_b32 s12, v65
	v_pk_fma_f32 v[60:61], v[94:95], v[94:95], v[60:61]
	v_mov_b32_e32 v24, v48
	v_mov_b32_e32 v64, v62
	v_mov_b32_e32 v65, v25
	v_mul_f32_e32 v4, v23, v23
	v_pk_add_f32 v[48:49], v[48:49], v[62:63]
	v_pk_mul_f32 v[62:63], v[24:25], v[64:65]
	v_pk_add_f32 v[60:61], v[60:61], v[60:61] op_sel:[0,1] op_sel_hi:[1,0]
	v_mov_b32_e32 v49, v63
	v_mov_b32_e32 v61, v4
	v_mul_f32_e32 v2, v91, v91
	v_pk_add_f32 v[48:49], v[48:49], v[60:61]
	v_pk_fma_f32 v[60:61], v[90:91], v[90:91], v[2:3] op_sel_hi:[1,1,0]
	v_mul_f32_e32 v2, v97, v97
	v_mul_f32_e32 v18, v27, v27
	v_pk_fma_f32 v[62:63], v[96:97], v[96:97], v[2:3] op_sel_hi:[1,1,0]
	v_and_b32_e32 v107, 0xffff0000, v47
	v_mov_b32_e32 v63, v18
	v_and_b32_e32 v106, 0xffff0000, v46
	v_lshlrev_b32_e32 v105, 16, v47
	v_lshlrev_b32_e32 v104, 16, v46
	v_pk_mul_f32 v[46:47], v[106:107], v[106:107]
	v_and_b32_e32 v93, 0xffff0000, v45
	v_pk_fma_f32 v[46:47], v[104:105], v[104:105], v[46:47]
	v_and_b32_e32 v92, 0xffff0000, v44
	v_pk_add_f32 v[46:47], v[46:47], v[46:47] op_sel:[0,1] op_sel_hi:[1,0]
	v_lshlrev_b32_e32 v89, 16, v45
	v_lshlrev_b32_e32 v88, 16, v44
	v_pk_mul_f32 v[44:45], v[92:93], v[92:93]
	v_lshlrev_b32_e32 v78, 16, v42
	v_and_b32_e32 v79, 0xffff0000, v42
	v_lshlrev_b32_e32 v80, 16, v43
	v_and_b32_e32 v81, 0xffff0000, v43
	v_pk_fma_f32 v[44:45], v[88:89], v[88:89], v[44:45]
	v_mul_f32_e32 v2, v19, v19
	v_pk_add_f32 v[44:45], v[44:45], v[44:45] op_sel:[0,1] op_sel_hi:[1,0]
	s_add_u32 s52, s9, s46
	v_mov_b32_e32 v45, v2
	v_mul_f32_e32 v2, v79, v79
	s_addc_u32 s53, s12, s47
	s_add_u32 s58, s2, 0x6000
	v_mul_f32_e32 v4, v58, v58
	s_addc_u32 s59, s3, 0
	s_add_u32 s60, s2, 0x8000
	s_addc_u32 s61, s3, 0
	s_add_u32 s54, s0, 0x6000
	s_addc_u32 s55, s1, 0
	s_add_u32 s56, s0, 0x8000
	s_mov_b32 s0, 0x3a000000
	s_addc_u32 s57, s1, 0
	v_mov_b32_e32 v22, v25
	s_waitcnt vmcnt(7)
	v_and_b32_e32 v73, 0xffff0000, v41
	v_and_b32_e32 v71, 0xffff0000, v40
	v_lshlrev_b32_e32 v72, 16, v41
	s_waitcnt vmcnt(4)
	v_mov_b32_e32 v6, v250
	v_mov_b32_e32 v7, v251
	v_lshlrev_b32_e32 v55, 16, v6
	v_and_b32_e32 v53, 0xffff0000, v6
	v_mul_f32_e32 v6, v26, v26
	v_mov_b32_e32 v61, v6
	v_pk_add_f32 v[60:61], v[60:61], v[62:63]
	v_mul_f32_e32 v6, v59, v59
	v_pk_add_f32 v[48:49], v[48:49], v[60:61]
	v_lshlrev_b32_e32 v70, 16, v40
	v_pk_add_f32 v[42:43], v[48:49], v[48:49] op_sel:[0,1] op_sel_hi:[1,0]
	v_mov_b32_e32 v48, v46
	v_mov_b32_e32 v20, v42
	v_mov_b32_e32 v49, v21
	v_pk_add_f32 v[42:43], v[42:43], v[46:47]
	v_pk_mul_f32 v[46:47], v[20:21], v[48:49]
	v_and_b32_e32 v77, 0xffff0000, v39
	v_mov_b32_e32 v43, v47
	v_pk_add_f32 v[42:43], v[42:43], v[44:45]
	v_pk_fma_f32 v[44:45], v[78:79], v[78:79], v[2:3] op_sel_hi:[1,1,0]
	v_mul_f32_e32 v2, v81, v81
	v_pk_fma_f32 v[46:47], v[80:81], v[80:81], v[2:3] op_sel_hi:[1,1,0]
	v_mov_b32_e32 v45, v4
	v_mov_b32_e32 v47, v6
	v_pk_add_f32 v[44:45], v[44:45], v[46:47]
	v_mul_f32_e32 v2, v73, v73
	v_pk_add_f32 v[108:109], v[42:43], v[44:45]
	global_load_dwordx4 v[118:121], v181, s[52:53]
	global_load_dwordx4 v[122:125], v181, s[60:61]
	global_load_dwordx4 v[126:129], v181, s[58:59]
	global_load_dwordx4 v[130:133], v181, s[52:53] offset:1024
	global_load_dwordx4 v[134:137], v182, s[60:61]
	global_load_dwordx4 v[138:141], v182, s[58:59]
	global_load_dwordx4 v[142:145], v181, s[52:53] offset:2048
	global_load_dwordx4 v[146:149], v183, s[60:61]
	global_load_dwordx4 v[150:153], v183, s[58:59]
	global_load_dwordx4 v[154:157], v181, s[52:53] offset:3072
	global_load_dwordx4 v[158:161], v184, s[60:61]
	global_load_dwordx4 v[162:165], v184, s[58:59]
	global_load_dwordx4 v[166:169], v185, s[52:53]
	global_load_dwordx4 v[170:173], v185, s[60:61]
	global_load_dwordx4 v[174:177], v185, s[58:59]
	global_load_dwordx4 v[214:217], v186, s[52:53]
	global_load_dwordx4 v[224:227], v186, s[60:61]
	global_load_dwordx4 v[228:231], v186, s[58:59]
	global_load_dwordx4 v[232:235], v187, s[52:53]
	global_load_dwordx4 v[236:239], v187, s[60:61]
	global_load_dwordx4 v[240:243], v187, s[58:59]
	global_load_dwordx4 v[244:247], v190, s[52:53]
	global_load_dwordx4 v[248:251], v190, s[60:61]
	v_pk_fma_f32 v[40:41], v[72:73], v[72:73], v[2:3] op_sel_hi:[1,1,0]
	v_and_b32_e32 v76, 0xffff0000, v38
	v_mul_f32_e32 v2, v71, v71
	v_lshlrev_b32_e32 v75, 16, v39
	v_lshlrev_b32_e32 v74, 16, v38
	v_pk_mul_f32 v[38:39], v[76:77], v[76:77]
	v_lshlrev_b32_e32 v62, 16, v36
	v_and_b32_e32 v63, 0xffff0000, v36
	v_lshlrev_b32_e32 v64, 16, v37
	v_and_b32_e32 v65, 0xffff0000, v37
	v_pk_fma_f32 v[36:37], v[70:71], v[70:71], v[2:3] op_sel_hi:[1,1,0]
	v_pk_fma_f32 v[38:39], v[74:75], v[74:75], v[38:39]
	v_mov_b32_e32 v54, v36
	v_mul_f32_e32 v4, v53, v53
	v_pk_add_f32 v[36:37], v[36:37], v[40:41]
	v_pk_add_f32 v[38:39], v[38:39], v[38:39] op_sel:[0,1] op_sel_hi:[1,0]
	v_mul_f32_e32 v2, v63, v63
	v_mov_b32_e32 v39, v4
	v_lshlrev_b32_e32 v56, 16, v7
	v_and_b32_e32 v57, 0xffff0000, v7
	v_mul_f32_e32 v6, v56, v56
	v_mul_f32_e32 v18, v57, v57
	s_waitcnt vmcnt(26)
	v_and_b32_e32 v69, 0xffff0000, v35
	v_and_b32_e32 v68, 0xffff0000, v34
	v_lshlrev_b32_e32 v67, 16, v35
	v_lshlrev_b32_e32 v66, 16, v34
	v_pk_mul_f32 v[34:35], v[68:69], v[68:69]
	s_waitcnt vmcnt(25)
	v_and_b32_e32 v87, 0xffff0000, v33
	v_pk_fma_f32 v[34:35], v[66:67], v[66:67], v[34:35]
	v_and_b32_e32 v86, 0xffff0000, v32
	s_waitcnt vmcnt(23)
	v_lshlrev_b32_e32 v7, 16, v50
	v_pk_add_f32 v[34:35], v[34:35], v[34:35] op_sel:[0,1] op_sel_hi:[1,0]
	v_lshlrev_b32_e32 v61, 16, v33
	v_lshlrev_b32_e32 v60, 16, v32
	v_pk_mul_f32 v[32:33], v[86:87], v[86:87]
	v_lshlrev_b32_e32 v82, 16, v30
	v_and_b32_e32 v83, 0xffff0000, v30
	v_lshlrev_b32_e32 v84, 16, v31
	v_and_b32_e32 v85, 0xffff0000, v31
	v_and_b32_e32 v5, 0xffff0000, v50
	v_pk_fma_f32 v[32:33], v[60:61], v[60:61], v[32:33]
	v_lshlrev_b32_e32 v50, 16, v51
	v_pk_add_f32 v[32:33], v[32:33], v[32:33] op_sel:[0,1] op_sel_hi:[1,0]
	v_and_b32_e32 v51, 0xffff0000, v51
	v_mul_f32_e32 v4, v50, v50
	v_mov_b32_e32 v52, v55
	s_waitcnt vmcnt(21)
	v_mov_b32_e32 v42, v118
	v_mov_b32_e32 v43, v119
	v_mov_b32_e32 v44, v120
	v_mov_b32_e32 v45, v121
	v_mov_b32_e32 v46, v122
	v_mov_b32_e32 v47, v123
	v_mov_b32_e32 v48, v124
	v_mov_b32_e32 v49, v125
	global_load_dwordx4 v[118:121], v190, s[58:59]
	global_load_dwordx4 v[122:125], v181, s[52:53]
	v_pk_add_f32 v[212:213], v[46:47], 1.0 op_sel_hi:[1,0]
	v_mov_b32_e32 v46, v40
	v_mov_b32_e32 v47, v55
	v_pk_mul_f32 v[40:41], v[54:55], v[46:47]
	v_pk_add_f32 v[48:49], v[48:49], 1.0 op_sel_hi:[1,0]
	v_mov_b32_e32 v37, v41
	v_pk_add_f32 v[36:37], v[36:37], v[38:39]
	v_pk_fma_f32 v[38:39], v[62:63], v[62:63], v[2:3] op_sel_hi:[1,1,0]
	v_mul_f32_e32 v2, v65, v65
	v_pk_fma_f32 v[40:41], v[64:65], v[64:65], v[2:3] op_sel_hi:[1,1,0]
	v_mov_b32_e32 v39, v6
	v_mov_b32_e32 v41, v18
	v_pk_add_f32 v[38:39], v[38:39], v[40:41]
	v_mul_f32_e32 v2, v5, v5
	v_pk_add_f32 v[36:37], v[36:37], v[38:39]
	v_mov_b32_e32 v33, v2
	v_pk_add_f32 v[30:31], v[36:37], v[36:37] op_sel:[0,1] op_sel_hi:[1,0]
	v_mov_b32_e32 v36, v34
	v_mov_b32_e32 v6, v30
	v_mov_b32_e32 v37, v7
	v_pk_add_f32 v[30:31], v[30:31], v[34:35]
	v_pk_mul_f32 v[34:35], v[6:7], v[36:37]
	v_mul_f32_e32 v2, v83, v83
	v_mov_b32_e32 v31, v35
	v_pk_add_f32 v[30:31], v[30:31], v[32:33]
	v_pk_fma_f32 v[32:33], v[82:83], v[82:83], v[2:3] op_sel_hi:[1,1,0]
	v_mul_f32_e32 v2, v85, v85
	v_mul_f32_e32 v18, v51, v51
	v_pk_fma_f32 v[34:35], v[84:85], v[84:85], v[2:3] op_sel_hi:[1,1,0]
	v_mov_b32_e32 v33, v4
	v_mov_b32_e32 v35, v18
	v_pk_add_f32 v[32:33], v[32:33], v[34:35]
	v_mov_b32_e32 v40, v95
	v_pk_add_f32 v[30:31], v[30:31], v[32:33]
	v_mov_b32_e32 v33, v108
	v_mov_b32_e32 v32, v30
	v_mov_b32_e32 v108, v31
	v_pk_add_f32 v[30:31], v[32:33], v[108:109]
	v_mov_b32_e32 v41, v99
	v_mov_b32_e32 v95, v98
	v_mov_b32_dpp v33, v31 quad_perm:[1,0,3,2] row_mask:0xf bank_mask:0xf bound_ctrl:1
	v_mov_b32_dpp v32, v30 quad_perm:[1,0,3,2] row_mask:0xf bank_mask:0xf bound_ctrl:1
	v_pk_add_f32 v[30:31], v[30:31], v[32:33]
	v_mov_b32_e32 v18, v21
	s_nop 0
	v_mov_b32_dpp v33, v31 quad_perm:[2,3,0,1] row_mask:0xf bank_mask:0xf bound_ctrl:1
	v_mov_b32_dpp v32, v30 quad_perm:[2,3,0,1] row_mask:0xf bank_mask:0xf bound_ctrl:1
	v_pk_add_f32 v[30:31], v[30:31], v[32:33]
	s_nop 1
	v_mov_b32_dpp v33, v31 row_half_mirror row_mask:0xf bank_mask:0xf bound_ctrl:1
	v_mov_b32_dpp v32, v30 row_half_mirror row_mask:0xf bank_mask:0xf bound_ctrl:1
	v_pk_add_f32 v[30:31], v[30:31], v[32:33]
	s_nop 1
	v_mov_b32_dpp v33, v31 row_mirror row_mask:0xf bank_mask:0xf bound_ctrl:1
	v_mov_b32_dpp v32, v30 row_mirror row_mask:0xf bank_mask:0xf bound_ctrl:1
	v_pk_add_f32 v[30:31], v[30:31], v[32:33]
	ds_bpermute_b32 v33, v111, v31
	ds_bpermute_b32 v32, v111, v30
	s_waitcnt lgkmcnt(0)
	v_pk_add_f32 v[30:31], v[30:31], v[32:33]
	ds_bpermute_b32 v33, v112, v31
	ds_bpermute_b32 v32, v112, v30
	s_waitcnt lgkmcnt(0)
	v_pk_add_f32 v[30:31], v[30:31], v[32:33]
	s_nop 0
	v_pk_fma_f32 v[108:109], v[30:31], s[0:1], v[188:189] op_sel_hi:[1,0,0]
	s_nop 0
	v_mul_f32_e32 v2, 0x4b800000, v109
	v_cmp_gt_f32_e64 s[0:1], s11, v109
	v_cmp_gt_f32_e32 vcc, s11, v108
	s_nop 0
	v_cndmask_b32_e64 v2, v109, v2, s[0:1]
	v_rsq_f32_e32 v2, v2
	s_nop 0
	v_mul_f32_e32 v4, 0x45800000, v2
	v_cndmask_b32_e64 v2, v2, v4, s[0:1]
	v_pk_mul_f32 v[30:31], v[2:3], v[102:103] op_sel_hi:[0,1]
	v_pk_mul_f32 v[32:33], v[2:3], v[100:101] op_sel_hi:[0,1]
	v_pk_mul_f32 v[32:33], v[42:43], v[32:33]
	v_pk_mul_f32 v[30:31], v[44:45], v[30:31]
	s_mov_b32 s0, 0x40200000
	s_waitcnt vmcnt(22)
	v_mov_b32_e32 v192, v126
	v_mov_b32_e32 v193, v127
	v_mov_b32_e32 v194, v128
	v_mov_b32_e32 v195, v129
	global_load_dwordx4 v[126:129], v181, s[56:57]
	v_pk_fma_f32 v[46:47], v[48:49], v[30:31], v[194:195]
	v_pk_fma_f32 v[48:49], v[212:213], v[32:33], v[192:193]
	v_add_co_u32_e64 v100, s[0:1], s0, v28
	v_cvt_pk_bf16_f32 v30, v48, v49
	v_cvt_pk_bf16_f32 v31, v46, v47
	v_addc_co_u32_e64 v101, s[0:1], 0, v29, s[0:1]
	global_store_dwordx2 v[100:101], v[30:31], off
	s_nop 0
	v_pk_mul_f32 v[40:41], v[2:3], v[40:41] op_sel_hi:[0,1]
	v_pk_mul_f32 v[42:43], v[2:3], v[94:95] op_sel_hi:[0,1]
	v_pk_mul_f32 v[90:91], v[2:3], v[90:91] op_sel_hi:[0,1]
	v_pk_mul_f32 v[26:27], v[2:3], v[26:27] op_sel_hi:[0,1]
	v_pk_mul_f32 v[22:23], v[2:3], v[22:23] op_sel_hi:[0,1]
	v_pk_mul_f32 v[80:81], v[2:3], v[80:81] op_sel_hi:[0,1]
	v_pk_mul_f32 v[78:79], v[2:3], v[78:79] op_sel_hi:[0,1]
	v_pk_mul_f32 v[58:59], v[2:3], v[58:59] op_sel_hi:[0,1]
	v_pk_mul_f32 v[18:19], v[2:3], v[18:19] op_sel_hi:[0,1]
	s_waitcnt vmcnt(23)
	v_mov_b32_e32 v28, v130
	v_mov_b32_e32 v29, v131
	v_mov_b32_e32 v30, v132
	v_mov_b32_e32 v31, v133
	global_load_dwordx4 v[130:133], v181, s[54:55]
	v_pk_mul_f32 v[28:29], v[28:29], v[42:43]
	v_pk_mul_f32 v[30:31], v[30:31], v[40:41]
	s_waitcnt vmcnt(23)
	v_mov_b32_e32 v32, v134
	v_mov_b32_e32 v33, v135
	v_mov_b32_e32 v34, v136
	v_mov_b32_e32 v35, v137
	global_load_dwordx4 v[134:137], v181, s[52:53] offset:1024
	v_pk_add_f32 v[34:35], v[34:35], 1.0 op_sel_hi:[1,0]
	v_pk_add_f32 v[32:33], v[32:33], 1.0 op_sel_hi:[1,0]
	s_waitcnt vmcnt(23)
	v_mov_b32_e32 v36, v138
	v_mov_b32_e32 v37, v139
	v_mov_b32_e32 v38, v140
	v_mov_b32_e32 v39, v141
	global_load_dwordx4 v[138:141], v182, s[56:57]
	v_pk_fma_f32 v[42:43], v[34:35], v[30:31], v[38:39]
	v_pk_fma_f32 v[44:45], v[32:33], v[28:29], v[36:37]
	v_cvt_pk_bf16_f32 v29, v42, v43
	v_cvt_pk_bf16_f32 v28, v44, v45
	global_store_dwordx2 v[100:101], v[28:29], off offset:512
	s_nop 0
	v_pk_mul_f32 v[40:41], v[2:3], v[96:97] op_sel_hi:[0,1]
	s_waitcnt vmcnt(24)
	v_mov_b32_e32 v28, v142
	v_mov_b32_e32 v29, v143
	v_mov_b32_e32 v30, v144
	v_mov_b32_e32 v31, v145
	global_load_dwordx4 v[142:145], v182, s[54:55]
	v_pk_mul_f32 v[28:29], v[28:29], v[90:91]
	v_pk_mul_f32 v[30:31], v[30:31], v[40:41]
	s_waitcnt vmcnt(24)
	v_mov_b32_e32 v32, v146
	v_mov_b32_e32 v33, v147
	v_mov_b32_e32 v34, v148
	v_mov_b32_e32 v35, v149
	global_load_dwordx4 v[146:149], v181, s[52:53] offset:2048
	v_pk_add_f32 v[34:35], v[34:35], 1.0 op_sel_hi:[1,0]
	v_pk_add_f32 v[32:33], v[32:33], 1.0 op_sel_hi:[1,0]
	s_waitcnt vmcnt(24)
	v_mov_b32_e32 v36, v150
	v_mov_b32_e32 v37, v151
	v_mov_b32_e32 v38, v152
	v_mov_b32_e32 v39, v153
	global_load_dwordx4 v[150:153], v183, s[56:57]
	v_pk_fma_f32 v[38:39], v[34:35], v[30:31], v[38:39]
	v_pk_fma_f32 v[40:41], v[32:33], v[28:29], v[36:37]
	v_cvt_pk_bf16_f32 v29, v38, v39
	v_cvt_pk_bf16_f32 v28, v40, v41
	global_store_dwordx2 v[100:101], v[28:29], off offset:1024
	s_nop 0
	v_mov_b32_e32 v90, v89
	v_mov_b32_e32 v91, v93
	v_mov_b32_e32 v89, v92
	v_pk_mul_f32 v[90:91], v[2:3], v[90:91] op_sel_hi:[0,1]
	v_pk_mul_f32 v[88:89], v[2:3], v[88:89] op_sel_hi:[0,1]
	s_waitcnt vmcnt(25)
	v_mov_b32_e32 v28, v154
	v_mov_b32_e32 v29, v155
	v_mov_b32_e32 v30, v156
	v_mov_b32_e32 v31, v157
	global_load_dwordx4 v[154:157], v183, s[54:55]
	v_pk_mul_f32 v[22:23], v[22:23], v[28:29]
	v_pk_mul_f32 v[24:25], v[26:27], v[30:31]
	s_waitcnt vmcnt(25)
	v_mov_b32_e32 v32, v158
	v_mov_b32_e32 v33, v159
	v_mov_b32_e32 v34, v160
	v_mov_b32_e32 v35, v161
	global_load_dwordx4 v[158:161], v181, s[52:53] offset:3072
	v_pk_add_f32 v[26:27], v[34:35], 1.0 op_sel_hi:[1,0]
	v_pk_add_f32 v[28:29], v[32:33], 1.0 op_sel_hi:[1,0]
	s_waitcnt vmcnt(25)
	v_mov_b32_e32 v94, v162
	v_mov_b32_e32 v95, v163
	v_mov_b32_e32 v96, v164
	v_mov_b32_e32 v97, v165
	global_load_dwordx4 v[162:165], v184, s[56:57]
	v_pk_fma_f32 v[30:31], v[24:25], v[26:27], v[96:97]
	v_pk_fma_f32 v[32:33], v[22:23], v[28:29], v[94:95]
	v_cvt_pk_bf16_f32 v23, v30, v31
	v_cvt_pk_bf16_f32 v22, v32, v33
	global_store_dwordx2 v[100:101], v[22:23], off offset:1536
	s_nop 0
	v_mov_b32_e32 v34, v105
	v_mov_b32_e32 v35, v107
	v_mov_b32_e32 v105, v106
	v_pk_mul_f32 v[34:35], v[2:3], v[34:35] op_sel_hi:[0,1]
	v_pk_mul_f32 v[36:37], v[2:3], v[104:105] op_sel_hi:[0,1]
	v_mul_f32_e32 v2, 0x4b800000, v108
	v_cndmask_b32_e32 v2, v108, v2, vcc
	v_rsq_f32_e32 v2, v2
	s_waitcnt vmcnt(26)
	v_mov_b32_e32 v22, v166
	v_mov_b32_e32 v23, v167
	v_mov_b32_e32 v24, v168
	v_mov_b32_e32 v25, v169
	global_load_dwordx4 v[166:169], v184, s[54:55]
	v_pk_mul_f32 v[22:23], v[36:37], v[22:23]
	v_pk_mul_f32 v[24:25], v[34:35], v[24:25]
	s_waitcnt vmcnt(26)
	v_mov_b32_e32 v26, v170
	v_mov_b32_e32 v27, v171
	v_mov_b32_e32 v28, v172
	v_mov_b32_e32 v29, v173
	global_load_dwordx4 v[170:173], v185, s[52:53]
	v_pk_add_f32 v[28:29], v[28:29], 1.0 op_sel_hi:[1,0]
	v_pk_add_f32 v[26:27], v[26:27], 1.0 op_sel_hi:[1,0]
	s_waitcnt vmcnt(26)
	v_mov_b32_e32 v94, v174
	v_mov_b32_e32 v95, v175
	v_mov_b32_e32 v96, v176
	v_mov_b32_e32 v97, v177
	global_load_dwordx4 v[174:177], v185, s[56:57]
	v_pk_fma_f32 v[34:35], v[24:25], v[28:29], v[96:97]
	v_pk_fma_f32 v[36:37], v[22:23], v[26:27], v[94:95]
	v_cvt_pk_bf16_f32 v23, v34, v35
	v_cvt_pk_bf16_f32 v22, v36, v37
	global_store_dwordx2 v[100:101], v[22:23], off offset:2048
	s_nop 0
	v_mul_f32_e32 v4, 0x45800000, v2
	v_cndmask_b32_e32 v2, v2, v4, vcc
	v_pk_mul_f32 v[70:71], v[2:3], v[70:71] op_sel_hi:[0,1]
	v_pk_mul_f32 v[62:63], v[2:3], v[62:63] op_sel_hi:[0,1]
	v_pk_mul_f32 v[56:57], v[2:3], v[56:57] op_sel_hi:[0,1]
	v_pk_mul_f32 v[52:53], v[2:3], v[52:53] op_sel_hi:[0,1]
	v_pk_mul_f32 v[82:83], v[2:3], v[82:83] op_sel_hi:[0,1]
	v_mov_b32_e32 v4, v7
	v_pk_mul_f32 v[50:51], v[2:3], v[50:51] op_sel_hi:[0,1]
	v_pk_mul_f32 v[4:5], v[2:3], v[4:5] op_sel_hi:[0,1]
	s_waitcnt vmcnt(27)
	v_mov_b32_e32 v22, v214
	v_mov_b32_e32 v23, v215
	v_mov_b32_e32 v24, v216
	v_mov_b32_e32 v25, v217
	global_load_dwordx4 v[214:217], v185, s[54:55]
	v_pk_mul_f32 v[22:23], v[88:89], v[22:23]
	v_pk_mul_f32 v[24:25], v[90:91], v[24:25]
	s_waitcnt vmcnt(27)
	v_mov_b32_e32 v26, v224
	v_mov_b32_e32 v27, v225
	v_mov_b32_e32 v28, v226
	v_mov_b32_e32 v29, v227
	global_load_dwordx4 v[224:227], v186, s[52:53]
	v_pk_add_f32 v[28:29], v[28:29], 1.0 op_sel_hi:[1,0]
	v_pk_add_f32 v[88:89], v[26:27], 1.0 op_sel_hi:[1,0]
	s_waitcnt vmcnt(27)
	v_mov_b32_e32 v94, v228
	v_mov_b32_e32 v95, v229
	v_mov_b32_e32 v96, v230
	v_mov_b32_e32 v97, v231
	global_load_dwordx4 v[228:231], v186, s[56:57]
	v_pk_fma_f32 v[26:27], v[24:25], v[28:29], v[96:97]
	v_pk_fma_f32 v[28:29], v[22:23], v[88:89], v[94:95]
	v_cvt_pk_bf16_f32 v23, v26, v27
	v_cvt_pk_bf16_f32 v22, v28, v29
	global_store_dwordx2 v[100:101], v[22:23], off offset:2560
	s_nop 0
	v_lshl_add_u64 v[96:97], v[12:13], 0, s[50:51]
	s_waitcnt vmcnt(28)
	v_mov_b32_e32 v22, v232
	v_mov_b32_e32 v23, v233
	v_mov_b32_e32 v24, v234
	v_mov_b32_e32 v25, v235
	global_load_dwordx4 v[232:235], v186, s[54:55]
	v_pk_mul_f32 v[78:79], v[78:79], v[22:23]
	v_pk_mul_f32 v[22:23], v[80:81], v[24:25]
	s_waitcnt vmcnt(28)
	v_mov_b32_e32 v88, v236
	v_mov_b32_e32 v89, v237
	v_mov_b32_e32 v90, v238
	v_mov_b32_e32 v91, v239
	global_load_dwordx4 v[236:239], v187, s[52:53]
	v_pk_add_f32 v[24:25], v[90:91], 1.0 op_sel_hi:[1,0]
	v_pk_add_f32 v[80:81], v[88:89], 1.0 op_sel_hi:[1,0]
	s_waitcnt vmcnt(28)
	v_mov_b32_e32 v92, v240
	v_mov_b32_e32 v93, v241
	v_mov_b32_e32 v94, v242
	v_mov_b32_e32 v95, v243
	global_load_dwordx4 v[240:243], v187, s[56:57]
	v_pk_fma_f32 v[22:23], v[22:23], v[24:25], v[94:95]
	v_pk_fma_f32 v[24:25], v[78:79], v[80:81], v[92:93]
	v_cvt_pk_bf16_f32 v79, v22, v23
	v_cvt_pk_bf16_f32 v78, v24, v25
	global_store_dwordx2 v[100:101], v[78:79], off offset:3072
	s_nop 0
	s_waitcnt vmcnt(29)
	v_mov_b32_e32 v78, v244
	v_mov_b32_e32 v79, v245
	v_mov_b32_e32 v80, v246
	v_mov_b32_e32 v81, v247
	global_load_dwordx4 v[244:247], v187, s[54:55]
	v_pk_mul_f32 v[20:21], v[18:19], v[78:79]
	v_pk_mul_f32 v[18:19], v[58:59], v[80:81]
	s_waitcnt vmcnt(29)
	v_mov_b32_e32 v88, v248
	v_mov_b32_e32 v89, v249
	v_mov_b32_e32 v90, v250
	v_mov_b32_e32 v91, v251
	global_load_dwordx4 v[248:251], v190, s[52:53]
	v_pk_add_f32 v[58:59], v[90:91], 1.0 op_sel_hi:[1,0]
	v_pk_add_f32 v[78:79], v[88:89], 1.0 op_sel_hi:[1,0]
	s_waitcnt vmcnt(29)
	v_mov_b32_e32 v92, v118
	v_mov_b32_e32 v93, v119
	v_mov_b32_e32 v94, v120
	v_mov_b32_e32 v95, v121
	global_load_dwordx4 v[118:121], v190, s[56:57]
	v_pk_fma_f32 v[18:19], v[18:19], v[58:59], v[94:95]
	v_pk_fma_f32 v[20:21], v[20:21], v[78:79], v[92:93]
	v_cvt_pk_bf16_f32 v59, v18, v19
	v_cvt_pk_bf16_f32 v58, v20, v21
	global_store_dwordx2 v[100:101], v[58:59], off offset:3584
	v_pk_mul_f32 v[58:59], v[2:3], v[72:73] op_sel_hi:[0,1]
	s_waitcnt vmcnt(30)
	v_mov_b32_e32 v78, v122
	v_mov_b32_e32 v79, v123
	v_mov_b32_e32 v80, v124
	v_mov_b32_e32 v81, v125
	global_load_dwordx4 v[122:125], v190, s[54:55]
	v_pk_mul_f32 v[72:73], v[78:79], v[70:71]
	v_pk_mul_f32 v[58:59], v[80:81], v[58:59]
	s_waitcnt vmcnt(30)
	v_mov_b32_e32 v88, v126
	v_mov_b32_e32 v89, v127
	v_mov_b32_e32 v90, v128
	v_mov_b32_e32 v91, v129
	v_pk_add_f32 v[70:71], v[90:91], 1.0 op_sel_hi:[1,0]
	v_pk_add_f32 v[78:79], v[88:89], 1.0 op_sel_hi:[1,0]
	s_waitcnt vmcnt(28)
	v_mov_b32_e32 v92, v130
	v_mov_b32_e32 v93, v131
	v_mov_b32_e32 v94, v132
	v_mov_b32_e32 v95, v133
	v_pk_fma_f32 v[70:71], v[70:71], v[58:59], v[94:95]
	v_pk_fma_f32 v[72:73], v[78:79], v[72:73], v[92:93]
	v_cvt_pk_bf16_f32 v59, v70, v71
	v_cvt_pk_bf16_f32 v58, v72, v73
	global_store_dwordx2 v[96:97], v[58:59], off
	v_mov_b32_e32 v58, v75
	v_mov_b32_e32 v59, v77
	v_mov_b32_e32 v75, v76
	v_pk_mul_f32 v[58:59], v[2:3], v[58:59] op_sel_hi:[0,1]
	v_pk_mul_f32 v[74:75], v[2:3], v[74:75] op_sel_hi:[0,1]
	s_waitcnt vmcnt(28)
	v_mov_b32_e32 v78, v134
	v_mov_b32_e32 v79, v135
	v_mov_b32_e32 v80, v136
	v_mov_b32_e32 v81, v137
	v_pk_mul_f32 v[74:75], v[78:79], v[74:75]
	v_pk_mul_f32 v[58:59], v[80:81], v[58:59]
	s_waitcnt vmcnt(27)
	v_mov_b32_e32 v88, v138
	v_mov_b32_e32 v89, v139
	v_mov_b32_e32 v90, v140
	v_mov_b32_e32 v91, v141
	v_pk_add_f32 v[76:77], v[90:91], 1.0 op_sel_hi:[1,0]
	v_pk_add_f32 v[80:81], v[88:89], 1.0 op_sel_hi:[1,0]
	s_waitcnt vmcnt(25)
	v_mov_b32_e32 v92, v142
	v_mov_b32_e32 v93, v143
	v_mov_b32_e32 v94, v144
	v_mov_b32_e32 v95, v145
	v_pk_fma_f32 v[78:79], v[76:77], v[58:59], v[94:95]
	v_pk_fma_f32 v[80:81], v[80:81], v[74:75], v[92:93]
	v_cvt_pk_bf16_f32 v59, v78, v79
	v_cvt_pk_bf16_f32 v58, v80, v81
	global_store_dwordx2 v[96:97], v[58:59], off offset:512
	v_pk_mul_f32 v[58:59], v[2:3], v[64:65] op_sel_hi:[0,1]
	s_waitcnt vmcnt(25)
	v_mov_b32_e32 v74, v146
	v_mov_b32_e32 v75, v147
	v_mov_b32_e32 v76, v148
	v_mov_b32_e32 v77, v149
	v_pk_mul_f32 v[62:63], v[74:75], v[62:63]
	v_pk_mul_f32 v[58:59], v[76:77], v[58:59]
	s_waitcnt vmcnt(24)
	v_mov_b32_e32 v88, v150
	v_mov_b32_e32 v89, v151
	v_mov_b32_e32 v90, v152
	v_mov_b32_e32 v91, v153
	v_pk_add_f32 v[64:65], v[90:91], 1.0 op_sel_hi:[1,0]
	v_pk_add_f32 v[76:77], v[88:89], 1.0 op_sel_hi:[1,0]
	s_waitcnt vmcnt(22)
	v_mov_b32_e32 v92, v154
	v_mov_b32_e32 v93, v155
	v_mov_b32_e32 v94, v156
	v_mov_b32_e32 v95, v157
	v_pk_fma_f32 v[74:75], v[64:65], v[58:59], v[94:95]
	v_pk_fma_f32 v[76:77], v[76:77], v[62:63], v[92:93]
	v_cvt_pk_bf16_f32 v59, v74, v75
	v_cvt_pk_bf16_f32 v58, v76, v77
	global_store_dwordx2 v[96:97], v[58:59], off offset:1024
	s_waitcnt vmcnt(22)
	v_mov_b32_e32 v62, v158
	v_mov_b32_e32 v63, v159
	v_mov_b32_e32 v64, v160
	v_mov_b32_e32 v65, v161
	v_pk_mul_f32 v[52:53], v[52:53], v[62:63]
	v_pk_mul_f32 v[54:55], v[56:57], v[64:65]
	s_waitcnt vmcnt(21)
	v_mov_b32_e32 v88, v162
	v_mov_b32_e32 v89, v163
	v_mov_b32_e32 v90, v164
	v_mov_b32_e32 v91, v165
	v_pk_add_f32 v[56:57], v[90:91], 1.0 op_sel_hi:[1,0]
	v_pk_add_f32 v[58:59], v[88:89], 1.0 op_sel_hi:[1,0]
	s_waitcnt vmcnt(19)
	v_mov_b32_e32 v92, v166
	v_mov_b32_e32 v93, v167
	v_mov_b32_e32 v94, v168
	v_mov_b32_e32 v95, v169
	v_pk_fma_f32 v[62:63], v[54:55], v[56:57], v[94:95]
	v_pk_fma_f32 v[64:65], v[52:53], v[58:59], v[92:93]
	v_cvt_pk_bf16_f32 v53, v62, v63
	v_cvt_pk_bf16_f32 v52, v64, v65
	global_store_dwordx2 v[96:97], v[52:53], off offset:1536
	s_nop 0
	v_mov_b32_e32 v92, v67
	v_mov_b32_e32 v93, v69
	v_mov_b32_e32 v67, v68
	v_pk_mul_f32 v[92:93], v[2:3], v[92:93] op_sel_hi:[0,1]
	v_pk_mul_f32 v[66:67], v[2:3], v[66:67] op_sel_hi:[0,1]
	s_waitcnt vmcnt(19)
	v_mov_b32_e32 v52, v170
	v_mov_b32_e32 v53, v171
	v_mov_b32_e32 v54, v172
	v_mov_b32_e32 v55, v173
	v_pk_mul_f32 v[52:53], v[66:67], v[52:53]
	v_pk_mul_f32 v[54:55], v[92:93], v[54:55]
	s_waitcnt vmcnt(18)
	v_mov_b32_e32 v56, v174
	v_mov_b32_e32 v57, v175
	v_mov_b32_e32 v58, v176
	v_mov_b32_e32 v59, v177
	v_pk_add_f32 v[58:59], v[58:59], 1.0 op_sel_hi:[1,0]
	v_pk_add_f32 v[56:57], v[56:57], 1.0 op_sel_hi:[1,0]
	s_waitcnt vmcnt(16)
	v_mov_b32_e32 v88, v214
	v_mov_b32_e32 v89, v215
	v_mov_b32_e32 v90, v216
	v_mov_b32_e32 v91, v217
	v_pk_fma_f32 v[66:67], v[54:55], v[58:59], v[90:91]
	v_pk_fma_f32 v[68:69], v[52:53], v[56:57], v[88:89]
	v_cvt_pk_bf16_f32 v53, v66, v67
	v_cvt_pk_bf16_f32 v52, v68, v69
	global_store_dwordx2 v[96:97], v[52:53], off offset:2048
	s_nop 0
	v_mov_b32_e32 v92, v61
	v_mov_b32_e32 v93, v87
	v_mov_b32_e32 v61, v86
	v_pk_mul_f32 v[92:93], v[2:3], v[92:93] op_sel_hi:[0,1]
	v_pk_mul_f32 v[60:61], v[2:3], v[60:61] op_sel_hi:[0,1]
	s_waitcnt vmcnt(16)
	v_mov_b32_e32 v52, v224
	v_mov_b32_e32 v53, v225
	v_mov_b32_e32 v54, v226
	v_mov_b32_e32 v55, v227
	v_pk_mul_f32 v[52:53], v[60:61], v[52:53]
	v_pk_mul_f32 v[54:55], v[92:93], v[54:55]
	s_waitcnt vmcnt(15)
	v_mov_b32_e32 v56, v228
	v_mov_b32_e32 v57, v229
	v_mov_b32_e32 v58, v230
	v_mov_b32_e32 v59, v231
	v_pk_add_f32 v[58:59], v[58:59], 1.0 op_sel_hi:[1,0]
	v_pk_add_f32 v[56:57], v[56:57], 1.0 op_sel_hi:[1,0]
	s_waitcnt vmcnt(13)
	v_mov_b32_e32 v88, v232
	v_mov_b32_e32 v89, v233
	v_mov_b32_e32 v90, v234
	v_mov_b32_e32 v91, v235
	v_pk_fma_f32 v[58:59], v[54:55], v[58:59], v[90:91]
	v_pk_fma_f32 v[60:61], v[52:53], v[56:57], v[88:89]
	v_cvt_pk_bf16_f32 v53, v58, v59
	v_cvt_pk_bf16_f32 v52, v60, v61
	global_store_dwordx2 v[96:97], v[52:53], off offset:2560
	s_nop 0
	v_pk_mul_f32 v[56:57], v[2:3], v[84:85] op_sel_hi:[0,1]
	s_waitcnt vmcnt(13)
	v_mov_b32_e32 v52, v236
	v_mov_b32_e32 v53, v237
	v_mov_b32_e32 v54, v238
	v_mov_b32_e32 v55, v239
	v_pk_mul_f32 v[52:53], v[82:83], v[52:53]
	v_pk_mul_f32 v[54:55], v[56:57], v[54:55]
	s_waitcnt vmcnt(12)
	v_mov_b32_e32 v86, v240
	v_mov_b32_e32 v87, v241
	v_mov_b32_e32 v88, v242
	v_mov_b32_e32 v89, v243
	v_pk_add_f32 v[56:57], v[88:89], 1.0 op_sel_hi:[1,0]
	v_pk_add_f32 v[82:83], v[86:87], 1.0 op_sel_hi:[1,0]
	s_waitcnt vmcnt(10)
	v_mov_b32_e32 v90, v244
	v_mov_b32_e32 v91, v245
	v_mov_b32_e32 v92, v246
	v_mov_b32_e32 v93, v247
	v_pk_fma_f32 v[54:55], v[54:55], v[56:57], v[92:93]
	v_pk_fma_f32 v[56:57], v[52:53], v[82:83], v[90:91]
	v_cvt_pk_bf16_f32 v53, v54, v55
	v_cvt_pk_bf16_f32 v52, v56, v57
	global_store_dwordx2 v[96:97], v[52:53], off offset:3072
	s_waitcnt vmcnt(10)
	v_mov_b32_e32 v82, v248
	v_mov_b32_e32 v83, v249
	v_mov_b32_e32 v84, v250
	v_mov_b32_e32 v85, v251
	v_pk_mul_f32 v[4:5], v[4:5], v[82:83]
	v_pk_mul_f32 v[6:7], v[50:51], v[84:85]
	s_waitcnt vmcnt(9)
	v_mov_b32_e32 v86, v118
	v_mov_b32_e32 v87, v119
	v_mov_b32_e32 v88, v120
	v_mov_b32_e32 v89, v121
	v_pk_add_f32 v[50:51], v[88:89], 1.0 op_sel_hi:[1,0]
	v_pk_add_f32 v[52:53], v[86:87], 1.0 op_sel_hi:[1,0]
	s_waitcnt vmcnt(7)
	v_mov_b32_e32 v90, v122
	v_mov_b32_e32 v91, v123
	v_mov_b32_e32 v92, v124
	v_mov_b32_e32 v93, v125
	v_pk_fma_f32 v[50:51], v[6:7], v[50:51], v[92:93]
	v_pk_fma_f32 v[52:53], v[4:5], v[52:53], v[90:91]
	v_cvt_pk_bf16_f32 v5, v50, v51
	v_cvt_pk_bf16_f32 v4, v52, v53
	global_store_dwordx2 v[96:97], v[4:5], off offset:3584
	v_add_u32_e32 v118, 0x10400, v110
	v_add_u32_e32 v119, 0x10800, v110
	v_add_u32_e32 v120, 0x10c00, v110
	v_add_u32_e32 v121, 0x11000, v110
	v_add_u32_e32 v122, 0x11400, v110
	v_add_u32_e32 v123, 0x11800, v110
	v_add_u32_e32 v124, 0x11c00, v110
	v_add_u32_e32 v125, 0x12000, v110
	v_add_u32_e32 v126, 0x12400, v110
	v_add_u32_e32 v127, 0x12800, v110
	v_add_u32_e32 v128, 0x12c00, v110
	v_add_u32_e32 v129, 0x13000, v110
	v_add_u32_e32 v130, 0x13400, v110
	v_add_u32_e32 v131, 0x13800, v110
	v_add_u32_e32 v132, 0x13c00, v110
	v_add_u32_e32 v133, 0x14000, v110
	v_add_u32_e32 v134, 0x14400, v110
	v_add_u32_e32 v135, 0x14800, v110
	v_add_u32_e32 v136, 0x14c00, v110
	v_add_u32_e32 v137, 0x15000, v110
	v_add_u32_e32 v138, 0x15400, v110
	v_add_u32_e32 v139, 0x15800, v110
	v_add_u32_e32 v140, 0x15c00, v110
	v_add_u32_e32 v141, 0x16000, v110
	v_add_u32_e32 v142, 0x16400, v110
	v_add_u32_e32 v143, 0x16800, v110
	v_add_u32_e32 v144, 0x16c00, v110
	v_add_u32_e32 v145, 0x17000, v110
	v_add_u32_e32 v146, 0x17400, v110
	v_add_u32_e32 v147, 0x17800, v110
	v_add_u32_e32 v148, 0x17c00, v110
	v_add_u32_e32 v149, 0x18000, v110
	v_add_u32_e32 v150, 0x18400, v110
	v_add_u32_e32 v151, 0x18800, v110
	v_add_u32_e32 v152, 0x18c00, v110
	v_add_u32_e32 v153, 0x19000, v110
	v_add_u32_e32 v154, 0x19400, v110
	v_add_u32_e32 v155, 0x19800, v110
	v_add_u32_e32 v156, 0x19c00, v110
	v_add_u32_e32 v157, 0x1a000, v110
	v_add_u32_e32 v158, 0x1a400, v110
	v_add_u32_e32 v159, 0x1a800, v110
	v_add_u32_e32 v160, 0x1ac00, v110
	v_add_u32_e32 v161, 0x1b000, v110
	v_add_u32_e32 v162, 0x1b400, v110
	v_add_u32_e32 v163, 0x1b800, v110
	v_add_u32_e32 v164, 0x1bc00, v110
	v_add_u32_e32 v165, 0x1c000, v110
	v_add_u32_e32 v166, 0x1c400, v110
	v_add_u32_e32 v167, 0x1c800, v110
	v_add_u32_e32 v168, 0x1cc00, v110
	v_add_u32_e32 v169, 0x1d000, v110
	v_add_u32_e32 v170, 0x1d400, v110
	v_add_u32_e32 v171, 0x1d800, v110
	v_add_u32_e32 v172, 0x1dc00, v110
	v_add_u32_e32 v173, 0x1e000, v110
	v_add_u32_e32 v174, 0x1e400, v110
	v_add_u32_e32 v175, 0x1e800, v110
	v_add_u32_e32 v176, 0x1ec00, v110
	v_add_u32_e32 v177, 0x1f000, v110
	ds_read_b128 v[214:217], v110
	ds_read_b128 v[224:227], v110 offset:1024
	ds_read_b128 v[228:231], v110 offset:2048
	ds_read_b128 v[232:235], v110 offset:3072
	ds_read_b128 v[236:239], v110 offset:4096
	ds_read_b128 v[240:243], v110 offset:5120
	ds_read_b128 v[244:247], v110 offset:6144
	s_waitcnt lgkmcnt(6)
	v_pk_mul_f32 v[248:249], v[214:215], v[48:49]
	v_pk_mul_f32 v[250:251], v[214:215], v[72:73]
	v_pk_fma_f32 v[248:249], v[216:217], v[46:47], v[248:249]
	v_pk_fma_f32 v[250:251], v[216:217], v[70:71], v[250:251]
	ds_read_b128 v[214:217], v110 offset:7168
	s_waitcnt lgkmcnt(6)
	v_pk_fma_f32 v[248:249], v[224:225], v[44:45], v[248:249]
	v_pk_fma_f32 v[250:251], v[224:225], v[80:81], v[250:251]
	v_pk_fma_f32 v[248:249], v[226:227], v[42:43], v[248:249]
	v_pk_fma_f32 v[250:251], v[226:227], v[78:79], v[250:251]
	ds_read_b128 v[224:227], v110 offset:8192
	s_waitcnt lgkmcnt(6)
	v_pk_fma_f32 v[248:249], v[228:229], v[40:41], v[248:249]
	v_pk_fma_f32 v[250:251], v[228:229], v[76:77], v[250:251]
	v_pk_fma_f32 v[248:249], v[230:231], v[38:39], v[248:249]
	v_pk_fma_f32 v[250:251], v[230:231], v[74:75], v[250:251]
	ds_read_b128 v[228:231], v110 offset:9216
	s_waitcnt lgkmcnt(6)
	v_pk_fma_f32 v[248:249], v[232:233], v[32:33], v[248:249]
	v_pk_fma_f32 v[250:251], v[232:233], v[64:65], v[250:251]
	v_pk_fma_f32 v[248:249], v[234:235], v[30:31], v[248:249]
	v_pk_fma_f32 v[250:251], v[234:235], v[62:63], v[250:251]
	ds_read_b128 v[232:235], v110 offset:10240
	s_waitcnt lgkmcnt(6)
	v_pk_fma_f32 v[248:249], v[236:237], v[36:37], v[248:249]
	v_pk_fma_f32 v[250:251], v[236:237], v[68:69], v[250:251]
	v_pk_fma_f32 v[248:249], v[238:239], v[34:35], v[248:249]
	v_pk_fma_f32 v[250:251], v[238:239], v[66:67], v[250:251]
	ds_read_b128 v[236:239], v110 offset:11264
	s_waitcnt lgkmcnt(6)
	v_pk_fma_f32 v[248:249], v[240:241], v[28:29], v[248:249]
	v_pk_fma_f32 v[250:251], v[240:241], v[60:61], v[250:251]
	v_pk_fma_f32 v[248:249], v[242:243], v[26:27], v[248:249]
	v_pk_fma_f32 v[250:251], v[242:243], v[58:59], v[250:251]
	ds_read_b128 v[240:243], v110 offset:12288
	s_waitcnt lgkmcnt(6)
	v_pk_fma_f32 v[248:249], v[244:245], v[24:25], v[248:249]
	v_pk_fma_f32 v[250:251], v[244:245], v[56:57], v[250:251]
	v_pk_fma_f32 v[248:249], v[246:247], v[22:23], v[248:249]
	v_pk_fma_f32 v[250:251], v[246:247], v[54:55], v[250:251]
	ds_read_b128 v[244:247], v110 offset:13312
	s_waitcnt lgkmcnt(6)
	v_pk_fma_f32 v[248:249], v[214:215], v[20:21], v[248:249]
	v_pk_fma_f32 v[250:251], v[214:215], v[52:53], v[250:251]
	v_pk_fma_f32 v[248:249], v[216:217], v[18:19], v[248:249]
	v_pk_fma_f32 v[250:251], v[216:217], v[50:51], v[250:251]
	ds_read_b128 v[214:217], v110 offset:14336
	v_add_f32_e32 v2, v248, v249
	v_add_f32_e32 v82, v250, v251
	s_waitcnt lgkmcnt(6)
	v_pk_mul_f32 v[248:249], v[224:225], v[48:49]
	v_pk_mul_f32 v[250:251], v[224:225], v[72:73]
	v_pk_fma_f32 v[248:249], v[226:227], v[46:47], v[248:249]
	v_pk_fma_f32 v[250:251], v[226:227], v[70:71], v[250:251]
	ds_read_b128 v[224:227], v110 offset:15360
	s_waitcnt lgkmcnt(6)
	v_pk_fma_f32 v[248:249], v[228:229], v[44:45], v[248:249]
	v_pk_fma_f32 v[250:251], v[228:229], v[80:81], v[250:251]
	v_pk_fma_f32 v[248:249], v[230:231], v[42:43], v[248:249]
	v_pk_fma_f32 v[250:251], v[230:231], v[78:79], v[250:251]
	ds_read_b128 v[228:231], v110 offset:16384
	s_waitcnt lgkmcnt(6)
	v_pk_fma_f32 v[248:249], v[232:233], v[40:41], v[248:249]
	v_pk_fma_f32 v[250:251], v[232:233], v[76:77], v[250:251]
	v_pk_fma_f32 v[248:249], v[234:235], v[38:39], v[248:249]
	v_pk_fma_f32 v[250:251], v[234:235], v[74:75], v[250:251]
	ds_read_b128 v[232:235], v110 offset:17408
	s_waitcnt lgkmcnt(6)
	v_pk_fma_f32 v[248:249], v[236:237], v[32:33], v[248:249]
	v_pk_fma_f32 v[250:251], v[236:237], v[64:65], v[250:251]
	v_pk_fma_f32 v[248:249], v[238:239], v[30:31], v[248:249]
	v_pk_fma_f32 v[250:251], v[238:239], v[62:63], v[250:251]
	ds_read_b128 v[236:239], v110 offset:18432
	s_waitcnt lgkmcnt(6)
	v_pk_fma_f32 v[248:249], v[240:241], v[36:37], v[248:249]
	v_pk_fma_f32 v[250:251], v[240:241], v[68:69], v[250:251]
	v_pk_fma_f32 v[248:249], v[242:243], v[34:35], v[248:249]
	v_pk_fma_f32 v[250:251], v[242:243], v[66:67], v[250:251]
	ds_read_b128 v[240:243], v110 offset:19456
	s_waitcnt lgkmcnt(6)
	v_pk_fma_f32 v[248:249], v[244:245], v[28:29], v[248:249]
	v_pk_fma_f32 v[250:251], v[244:245], v[60:61], v[250:251]
	v_pk_fma_f32 v[248:249], v[246:247], v[26:27], v[248:249]
	v_pk_fma_f32 v[250:251], v[246:247], v[58:59], v[250:251]
	ds_read_b128 v[244:247], v110 offset:20480
	s_waitcnt lgkmcnt(6)
	v_pk_fma_f32 v[248:249], v[214:215], v[24:25], v[248:249]
	v_pk_fma_f32 v[250:251], v[214:215], v[56:57], v[250:251]
	v_pk_fma_f32 v[248:249], v[216:217], v[22:23], v[248:249]
	v_pk_fma_f32 v[250:251], v[216:217], v[54:55], v[250:251]
	ds_read_b128 v[214:217], v110 offset:21504
	s_waitcnt lgkmcnt(6)
	v_pk_fma_f32 v[248:249], v[224:225], v[20:21], v[248:249]
	v_pk_fma_f32 v[250:251], v[224:225], v[52:53], v[250:251]
	v_pk_fma_f32 v[248:249], v[226:227], v[18:19], v[248:249]
	v_pk_fma_f32 v[250:251], v[226:227], v[50:51], v[250:251]
	ds_read_b128 v[224:227], v110 offset:22528
	v_add_f32_e32 v83, v248, v249
	v_add_f32_e32 v84, v250, v251
	s_waitcnt lgkmcnt(6)
	v_pk_mul_f32 v[248:249], v[228:229], v[48:49]
	v_pk_mul_f32 v[250:251], v[228:229], v[72:73]
	v_pk_fma_f32 v[248:249], v[230:231], v[46:47], v[248:249]
	v_pk_fma_f32 v[250:251], v[230:231], v[70:71], v[250:251]
	ds_read_b128 v[228:231], v110 offset:23552
	s_waitcnt lgkmcnt(6)
	v_pk_fma_f32 v[248:249], v[232:233], v[44:45], v[248:249]
	v_pk_fma_f32 v[250:251], v[232:233], v[80:81], v[250:251]
	v_pk_fma_f32 v[248:249], v[234:235], v[42:43], v[248:249]
	v_pk_fma_f32 v[250:251], v[234:235], v[78:79], v[250:251]
	ds_read_b128 v[232:235], v110 offset:24576
	s_waitcnt lgkmcnt(6)
	v_pk_fma_f32 v[248:249], v[236:237], v[40:41], v[248:249]
	v_pk_fma_f32 v[250:251], v[236:237], v[76:77], v[250:251]
	v_pk_fma_f32 v[248:249], v[238:239], v[38:39], v[248:249]
	v_pk_fma_f32 v[250:251], v[238:239], v[74:75], v[250:251]
	ds_read_b128 v[236:239], v110 offset:25600
	s_waitcnt lgkmcnt(6)
	v_pk_fma_f32 v[248:249], v[240:241], v[32:33], v[248:249]
	v_pk_fma_f32 v[250:251], v[240:241], v[64:65], v[250:251]
	v_pk_fma_f32 v[248:249], v[242:243], v[30:31], v[248:249]
	v_pk_fma_f32 v[250:251], v[242:243], v[62:63], v[250:251]
	ds_read_b128 v[240:243], v110 offset:26624
	s_waitcnt lgkmcnt(6)
	v_pk_fma_f32 v[248:249], v[244:245], v[36:37], v[248:249]
	v_pk_fma_f32 v[250:251], v[244:245], v[68:69], v[250:251]
	v_pk_fma_f32 v[248:249], v[246:247], v[34:35], v[248:249]
	v_pk_fma_f32 v[250:251], v[246:247], v[66:67], v[250:251]
	ds_read_b128 v[244:247], v110 offset:27648
	s_waitcnt lgkmcnt(6)
	v_pk_fma_f32 v[248:249], v[214:215], v[28:29], v[248:249]
	v_pk_fma_f32 v[250:251], v[214:215], v[60:61], v[250:251]
	v_pk_fma_f32 v[248:249], v[216:217], v[26:27], v[248:249]
	v_pk_fma_f32 v[250:251], v[216:217], v[58:59], v[250:251]
	ds_read_b128 v[214:217], v110 offset:28672
	s_waitcnt lgkmcnt(6)
	v_pk_fma_f32 v[248:249], v[224:225], v[24:25], v[248:249]
	v_pk_fma_f32 v[250:251], v[224:225], v[56:57], v[250:251]
	v_pk_fma_f32 v[248:249], v[226:227], v[22:23], v[248:249]
	v_pk_fma_f32 v[250:251], v[226:227], v[54:55], v[250:251]
	ds_read_b128 v[224:227], v110 offset:29696
	s_waitcnt lgkmcnt(6)
	v_pk_fma_f32 v[248:249], v[228:229], v[20:21], v[248:249]
	v_pk_fma_f32 v[250:251], v[228:229], v[52:53], v[250:251]
	v_pk_fma_f32 v[248:249], v[230:231], v[18:19], v[248:249]
	v_pk_fma_f32 v[250:251], v[230:231], v[50:51], v[250:251]
	ds_read_b128 v[228:231], v110 offset:30720
	v_add_f32_e32 v85, v248, v249
	v_add_f32_e32 v86, v250, v251
	s_waitcnt lgkmcnt(6)
	v_pk_mul_f32 v[248:249], v[232:233], v[48:49]
	v_pk_mul_f32 v[250:251], v[232:233], v[72:73]
	v_pk_fma_f32 v[248:249], v[234:235], v[46:47], v[248:249]
	v_pk_fma_f32 v[250:251], v[234:235], v[70:71], v[250:251]
	ds_read_b128 v[232:235], v110 offset:31744
	s_waitcnt lgkmcnt(6)
	v_pk_fma_f32 v[248:249], v[236:237], v[44:45], v[248:249]
	v_pk_fma_f32 v[250:251], v[236:237], v[80:81], v[250:251]
	v_pk_fma_f32 v[248:249], v[238:239], v[42:43], v[248:249]
	v_pk_fma_f32 v[250:251], v[238:239], v[78:79], v[250:251]
	ds_read_b128 v[236:239], v110 offset:32768
	s_waitcnt lgkmcnt(6)
	v_pk_fma_f32 v[248:249], v[240:241], v[40:41], v[248:249]
	v_pk_fma_f32 v[250:251], v[240:241], v[76:77], v[250:251]
	v_pk_fma_f32 v[248:249], v[242:243], v[38:39], v[248:249]
	v_pk_fma_f32 v[250:251], v[242:243], v[74:75], v[250:251]
	ds_read_b128 v[240:243], v110 offset:33792
	s_waitcnt lgkmcnt(6)
	v_pk_fma_f32 v[248:249], v[244:245], v[32:33], v[248:249]
	v_pk_fma_f32 v[250:251], v[244:245], v[64:65], v[250:251]
	v_pk_fma_f32 v[248:249], v[246:247], v[30:31], v[248:249]
	v_pk_fma_f32 v[250:251], v[246:247], v[62:63], v[250:251]
	ds_read_b128 v[244:247], v110 offset:34816
	s_waitcnt lgkmcnt(6)
	v_pk_fma_f32 v[248:249], v[214:215], v[36:37], v[248:249]
	v_pk_fma_f32 v[250:251], v[214:215], v[68:69], v[250:251]
	v_pk_fma_f32 v[248:249], v[216:217], v[34:35], v[248:249]
	v_pk_fma_f32 v[250:251], v[216:217], v[66:67], v[250:251]
	ds_read_b128 v[214:217], v110 offset:35840
	s_waitcnt lgkmcnt(6)
	v_pk_fma_f32 v[248:249], v[224:225], v[28:29], v[248:249]
	v_pk_fma_f32 v[250:251], v[224:225], v[60:61], v[250:251]
	v_pk_fma_f32 v[248:249], v[226:227], v[26:27], v[248:249]
	v_pk_fma_f32 v[250:251], v[226:227], v[58:59], v[250:251]
	ds_read_b128 v[224:227], v110 offset:36864
	s_waitcnt lgkmcnt(6)
	v_pk_fma_f32 v[248:249], v[228:229], v[24:25], v[248:249]
	v_pk_fma_f32 v[250:251], v[228:229], v[56:57], v[250:251]
	v_pk_fma_f32 v[248:249], v[230:231], v[22:23], v[248:249]
	v_pk_fma_f32 v[250:251], v[230:231], v[54:55], v[250:251]
	ds_read_b128 v[228:231], v110 offset:37888
	s_waitcnt lgkmcnt(6)
	v_pk_fma_f32 v[248:249], v[232:233], v[20:21], v[248:249]
	v_pk_fma_f32 v[250:251], v[232:233], v[52:53], v[250:251]
	v_pk_fma_f32 v[248:249], v[234:235], v[18:19], v[248:249]
	v_pk_fma_f32 v[250:251], v[234:235], v[50:51], v[250:251]
	ds_read_b128 v[232:235], v110 offset:38912
	v_add_f32_e32 v87, v248, v249
	v_add_f32_e32 v88, v250, v251
	s_waitcnt lgkmcnt(6)
	v_pk_mul_f32 v[248:249], v[236:237], v[48:49]
	v_pk_mul_f32 v[250:251], v[236:237], v[72:73]
	v_pk_fma_f32 v[248:249], v[238:239], v[46:47], v[248:249]
	v_pk_fma_f32 v[250:251], v[238:239], v[70:71], v[250:251]
	ds_read_b128 v[236:239], v110 offset:39936
	s_waitcnt lgkmcnt(6)
	v_pk_fma_f32 v[248:249], v[240:241], v[44:45], v[248:249]
	v_pk_fma_f32 v[250:251], v[240:241], v[80:81], v[250:251]
	v_pk_fma_f32 v[248:249], v[242:243], v[42:43], v[248:249]
	v_pk_fma_f32 v[250:251], v[242:243], v[78:79], v[250:251]
	ds_read_b128 v[240:243], v110 offset:40960
	s_waitcnt lgkmcnt(6)
	v_pk_fma_f32 v[248:249], v[244:245], v[40:41], v[248:249]
	v_pk_fma_f32 v[250:251], v[244:245], v[76:77], v[250:251]
	v_pk_fma_f32 v[248:249], v[246:247], v[38:39], v[248:249]
	v_pk_fma_f32 v[250:251], v[246:247], v[74:75], v[250:251]
	ds_read_b128 v[244:247], v110 offset:41984
	s_waitcnt lgkmcnt(6)
	v_pk_fma_f32 v[248:249], v[214:215], v[32:33], v[248:249]
	v_pk_fma_f32 v[250:251], v[214:215], v[64:65], v[250:251]
	v_pk_fma_f32 v[248:249], v[216:217], v[30:31], v[248:249]
	v_pk_fma_f32 v[250:251], v[216:217], v[62:63], v[250:251]
	ds_read_b128 v[214:217], v110 offset:43008
	s_waitcnt lgkmcnt(6)
	v_pk_fma_f32 v[248:249], v[224:225], v[36:37], v[248:249]
	v_pk_fma_f32 v[250:251], v[224:225], v[68:69], v[250:251]
	v_pk_fma_f32 v[248:249], v[226:227], v[34:35], v[248:249]
	v_pk_fma_f32 v[250:251], v[226:227], v[66:67], v[250:251]
	ds_read_b128 v[224:227], v110 offset:44032
	s_waitcnt lgkmcnt(6)
	v_pk_fma_f32 v[248:249], v[228:229], v[28:29], v[248:249]
	v_pk_fma_f32 v[250:251], v[228:229], v[60:61], v[250:251]
	v_pk_fma_f32 v[248:249], v[230:231], v[26:27], v[248:249]
	v_pk_fma_f32 v[250:251], v[230:231], v[58:59], v[250:251]
	ds_read_b128 v[228:231], v110 offset:45056
	s_waitcnt lgkmcnt(6)
	v_pk_fma_f32 v[248:249], v[232:233], v[24:25], v[248:249]
	v_pk_fma_f32 v[250:251], v[232:233], v[56:57], v[250:251]
	v_pk_fma_f32 v[248:249], v[234:235], v[22:23], v[248:249]
	v_pk_fma_f32 v[250:251], v[234:235], v[54:55], v[250:251]
	ds_read_b128 v[232:235], v110 offset:46080
	s_waitcnt lgkmcnt(6)
	v_pk_fma_f32 v[248:249], v[236:237], v[20:21], v[248:249]
	v_pk_fma_f32 v[250:251], v[236:237], v[52:53], v[250:251]
	v_pk_fma_f32 v[248:249], v[238:239], v[18:19], v[248:249]
	v_pk_fma_f32 v[250:251], v[238:239], v[50:51], v[250:251]
	ds_read_b128 v[236:239], v110 offset:47104
	v_add_f32_e32 v89, v248, v249
	v_add_f32_e32 v90, v250, v251
	s_waitcnt lgkmcnt(6)
	v_pk_mul_f32 v[248:249], v[240:241], v[48:49]
	v_pk_mul_f32 v[250:251], v[240:241], v[72:73]
	v_pk_fma_f32 v[248:249], v[242:243], v[46:47], v[248:249]
	v_pk_fma_f32 v[250:251], v[242:243], v[70:71], v[250:251]
	ds_read_b128 v[240:243], v110 offset:48128
	s_waitcnt lgkmcnt(6)
	v_pk_fma_f32 v[248:249], v[244:245], v[44:45], v[248:249]
	v_pk_fma_f32 v[250:251], v[244:245], v[80:81], v[250:251]
	v_pk_fma_f32 v[248:249], v[246:247], v[42:43], v[248:249]
	v_pk_fma_f32 v[250:251], v[246:247], v[78:79], v[250:251]
	ds_read_b128 v[244:247], v110 offset:49152
	s_waitcnt lgkmcnt(6)
	v_pk_fma_f32 v[248:249], v[214:215], v[40:41], v[248:249]
	v_pk_fma_f32 v[250:251], v[214:215], v[76:77], v[250:251]
	v_pk_fma_f32 v[248:249], v[216:217], v[38:39], v[248:249]
	v_pk_fma_f32 v[250:251], v[216:217], v[74:75], v[250:251]
	ds_read_b128 v[214:217], v110 offset:50176
	s_waitcnt lgkmcnt(6)
	v_pk_fma_f32 v[248:249], v[224:225], v[32:33], v[248:249]
	v_pk_fma_f32 v[250:251], v[224:225], v[64:65], v[250:251]
	v_pk_fma_f32 v[248:249], v[226:227], v[30:31], v[248:249]
	v_pk_fma_f32 v[250:251], v[226:227], v[62:63], v[250:251]
	ds_read_b128 v[224:227], v110 offset:51200
	s_waitcnt lgkmcnt(6)
	v_pk_fma_f32 v[248:249], v[228:229], v[36:37], v[248:249]
	v_pk_fma_f32 v[250:251], v[228:229], v[68:69], v[250:251]
	v_pk_fma_f32 v[248:249], v[230:231], v[34:35], v[248:249]
	v_pk_fma_f32 v[250:251], v[230:231], v[66:67], v[250:251]
	ds_read_b128 v[228:231], v110 offset:52224
	s_waitcnt lgkmcnt(6)
	v_pk_fma_f32 v[248:249], v[232:233], v[28:29], v[248:249]
	v_pk_fma_f32 v[250:251], v[232:233], v[60:61], v[250:251]
	v_pk_fma_f32 v[248:249], v[234:235], v[26:27], v[248:249]
	v_pk_fma_f32 v[250:251], v[234:235], v[58:59], v[250:251]
	ds_read_b128 v[232:235], v110 offset:53248
	s_waitcnt lgkmcnt(6)
	v_pk_fma_f32 v[248:249], v[236:237], v[24:25], v[248:249]
	v_pk_fma_f32 v[250:251], v[236:237], v[56:57], v[250:251]
	v_pk_fma_f32 v[248:249], v[238:239], v[22:23], v[248:249]
	v_pk_fma_f32 v[250:251], v[238:239], v[54:55], v[250:251]
	ds_read_b128 v[236:239], v110 offset:54272
	s_waitcnt lgkmcnt(6)
	v_pk_fma_f32 v[248:249], v[240:241], v[20:21], v[248:249]
	v_pk_fma_f32 v[250:251], v[240:241], v[52:53], v[250:251]
	v_pk_fma_f32 v[248:249], v[242:243], v[18:19], v[248:249]
	v_pk_fma_f32 v[250:251], v[242:243], v[50:51], v[250:251]
	ds_read_b128 v[240:243], v110 offset:55296
	v_add_f32_e32 v91, v248, v249
	v_add_f32_e32 v92, v250, v251
	s_waitcnt lgkmcnt(6)
	v_pk_mul_f32 v[248:249], v[244:245], v[48:49]
	v_pk_mul_f32 v[250:251], v[244:245], v[72:73]
	v_pk_fma_f32 v[248:249], v[246:247], v[46:47], v[248:249]
	v_pk_fma_f32 v[250:251], v[246:247], v[70:71], v[250:251]
	ds_read_b128 v[244:247], v110 offset:56320
	s_waitcnt lgkmcnt(6)
	v_pk_fma_f32 v[248:249], v[214:215], v[44:45], v[248:249]
	v_pk_fma_f32 v[250:251], v[214:215], v[80:81], v[250:251]
	v_pk_fma_f32 v[248:249], v[216:217], v[42:43], v[248:249]
	v_pk_fma_f32 v[250:251], v[216:217], v[78:79], v[250:251]
	ds_read_b128 v[214:217], v110 offset:57344
	s_waitcnt lgkmcnt(6)
	v_pk_fma_f32 v[248:249], v[224:225], v[40:41], v[248:249]
	v_pk_fma_f32 v[250:251], v[224:225], v[76:77], v[250:251]
	v_pk_fma_f32 v[248:249], v[226:227], v[38:39], v[248:249]
	v_pk_fma_f32 v[250:251], v[226:227], v[74:75], v[250:251]
	ds_read_b128 v[224:227], v110 offset:58368
	s_waitcnt lgkmcnt(6)
	v_pk_fma_f32 v[248:249], v[228:229], v[32:33], v[248:249]
	v_pk_fma_f32 v[250:251], v[228:229], v[64:65], v[250:251]
	v_pk_fma_f32 v[248:249], v[230:231], v[30:31], v[248:249]
	v_pk_fma_f32 v[250:251], v[230:231], v[62:63], v[250:251]
	ds_read_b128 v[228:231], v110 offset:59392
	s_waitcnt lgkmcnt(6)
	v_pk_fma_f32 v[248:249], v[232:233], v[36:37], v[248:249]
	v_pk_fma_f32 v[250:251], v[232:233], v[68:69], v[250:251]
	v_pk_fma_f32 v[248:249], v[234:235], v[34:35], v[248:249]
	v_pk_fma_f32 v[250:251], v[234:235], v[66:67], v[250:251]
	ds_read_b128 v[232:235], v110 offset:60416
	s_waitcnt lgkmcnt(6)
	v_pk_fma_f32 v[248:249], v[236:237], v[28:29], v[248:249]
	v_pk_fma_f32 v[250:251], v[236:237], v[60:61], v[250:251]
	v_pk_fma_f32 v[248:249], v[238:239], v[26:27], v[248:249]
	v_pk_fma_f32 v[250:251], v[238:239], v[58:59], v[250:251]
	ds_read_b128 v[236:239], v110 offset:61440
	s_waitcnt lgkmcnt(6)
	v_pk_fma_f32 v[248:249], v[240:241], v[24:25], v[248:249]
	v_pk_fma_f32 v[250:251], v[240:241], v[56:57], v[250:251]
	v_pk_fma_f32 v[248:249], v[242:243], v[22:23], v[248:249]
	v_pk_fma_f32 v[250:251], v[242:243], v[54:55], v[250:251]
	ds_read_b128 v[240:243], v110 offset:62464
	s_waitcnt lgkmcnt(6)
	v_pk_fma_f32 v[248:249], v[244:245], v[20:21], v[248:249]
	v_pk_fma_f32 v[250:251], v[244:245], v[52:53], v[250:251]
	v_pk_fma_f32 v[248:249], v[246:247], v[18:19], v[248:249]
	v_pk_fma_f32 v[250:251], v[246:247], v[50:51], v[250:251]
	ds_read_b128 v[244:247], v110 offset:63488
	v_add_f32_e32 v93, v248, v249
	v_add_f32_e32 v94, v250, v251
	s_waitcnt lgkmcnt(6)
	v_pk_mul_f32 v[248:249], v[214:215], v[48:49]
	v_pk_mul_f32 v[250:251], v[214:215], v[72:73]
	v_pk_fma_f32 v[248:249], v[216:217], v[46:47], v[248:249]
	v_pk_fma_f32 v[250:251], v[216:217], v[70:71], v[250:251]
	ds_read_b128 v[214:217], v110 offset:64512
	s_waitcnt lgkmcnt(6)
	v_pk_fma_f32 v[248:249], v[224:225], v[44:45], v[248:249]
	v_pk_fma_f32 v[250:251], v[224:225], v[80:81], v[250:251]
	v_pk_fma_f32 v[248:249], v[226:227], v[42:43], v[248:249]
	v_pk_fma_f32 v[250:251], v[226:227], v[78:79], v[250:251]
	ds_read_b128 v[224:227], v117
	s_waitcnt lgkmcnt(6)
	v_pk_fma_f32 v[248:249], v[228:229], v[40:41], v[248:249]
	v_pk_fma_f32 v[250:251], v[228:229], v[76:77], v[250:251]
	v_pk_fma_f32 v[248:249], v[230:231], v[38:39], v[248:249]
	v_pk_fma_f32 v[250:251], v[230:231], v[74:75], v[250:251]
	ds_read_b128 v[228:231], v118
	s_waitcnt lgkmcnt(6)
	v_pk_fma_f32 v[248:249], v[232:233], v[32:33], v[248:249]
	v_pk_fma_f32 v[250:251], v[232:233], v[64:65], v[250:251]
	v_pk_fma_f32 v[248:249], v[234:235], v[30:31], v[248:249]
	v_pk_fma_f32 v[250:251], v[234:235], v[62:63], v[250:251]
	ds_read_b128 v[232:235], v119
	s_waitcnt lgkmcnt(6)
	v_pk_fma_f32 v[248:249], v[236:237], v[36:37], v[248:249]
	v_pk_fma_f32 v[250:251], v[236:237], v[68:69], v[250:251]
	v_pk_fma_f32 v[248:249], v[238:239], v[34:35], v[248:249]
	v_pk_fma_f32 v[250:251], v[238:239], v[66:67], v[250:251]
	ds_read_b128 v[236:239], v120
	s_waitcnt lgkmcnt(6)
	v_pk_fma_f32 v[248:249], v[240:241], v[28:29], v[248:249]
	v_pk_fma_f32 v[250:251], v[240:241], v[60:61], v[250:251]
	v_pk_fma_f32 v[248:249], v[242:243], v[26:27], v[248:249]
	v_pk_fma_f32 v[250:251], v[242:243], v[58:59], v[250:251]
	ds_read_b128 v[240:243], v121
	s_waitcnt lgkmcnt(6)
	v_pk_fma_f32 v[248:249], v[244:245], v[24:25], v[248:249]
	v_pk_fma_f32 v[250:251], v[244:245], v[56:57], v[250:251]
	v_pk_fma_f32 v[248:249], v[246:247], v[22:23], v[248:249]
	v_pk_fma_f32 v[250:251], v[246:247], v[54:55], v[250:251]
	ds_read_b128 v[244:247], v122
	s_waitcnt lgkmcnt(6)
	v_pk_fma_f32 v[248:249], v[214:215], v[20:21], v[248:249]
	v_pk_fma_f32 v[250:251], v[214:215], v[52:53], v[250:251]
	v_pk_fma_f32 v[248:249], v[216:217], v[18:19], v[248:249]
	v_pk_fma_f32 v[250:251], v[216:217], v[50:51], v[250:251]
	ds_read_b128 v[214:217], v123
	v_add_f32_e32 v95, v248, v249
	v_add_f32_e32 v96, v250, v251
	s_waitcnt lgkmcnt(6)
	v_pk_mul_f32 v[248:249], v[224:225], v[48:49]
	v_pk_mul_f32 v[250:251], v[224:225], v[72:73]
	v_pk_fma_f32 v[248:249], v[226:227], v[46:47], v[248:249]
	v_pk_fma_f32 v[250:251], v[226:227], v[70:71], v[250:251]
	ds_read_b128 v[224:227], v124
	s_waitcnt lgkmcnt(6)
	v_pk_fma_f32 v[248:249], v[228:229], v[44:45], v[248:249]
	v_pk_fma_f32 v[250:251], v[228:229], v[80:81], v[250:251]
	v_pk_fma_f32 v[248:249], v[230:231], v[42:43], v[248:249]
	v_pk_fma_f32 v[250:251], v[230:231], v[78:79], v[250:251]
	ds_read_b128 v[228:231], v125
	s_waitcnt lgkmcnt(6)
	v_pk_fma_f32 v[248:249], v[232:233], v[40:41], v[248:249]
	v_pk_fma_f32 v[250:251], v[232:233], v[76:77], v[250:251]
	v_pk_fma_f32 v[248:249], v[234:235], v[38:39], v[248:249]
	v_pk_fma_f32 v[250:251], v[234:235], v[74:75], v[250:251]
	ds_read_b128 v[232:235], v126
	s_waitcnt lgkmcnt(6)
	v_pk_fma_f32 v[248:249], v[236:237], v[32:33], v[248:249]
	v_pk_fma_f32 v[250:251], v[236:237], v[64:65], v[250:251]
	v_pk_fma_f32 v[248:249], v[238:239], v[30:31], v[248:249]
	v_pk_fma_f32 v[250:251], v[238:239], v[62:63], v[250:251]
	ds_read_b128 v[236:239], v127
	s_waitcnt lgkmcnt(6)
	v_pk_fma_f32 v[248:249], v[240:241], v[36:37], v[248:249]
	v_pk_fma_f32 v[250:251], v[240:241], v[68:69], v[250:251]
	v_pk_fma_f32 v[248:249], v[242:243], v[34:35], v[248:249]
	v_pk_fma_f32 v[250:251], v[242:243], v[66:67], v[250:251]
	ds_read_b128 v[240:243], v128
	s_waitcnt lgkmcnt(6)
	v_pk_fma_f32 v[248:249], v[244:245], v[28:29], v[248:249]
	v_pk_fma_f32 v[250:251], v[244:245], v[60:61], v[250:251]
	v_pk_fma_f32 v[248:249], v[246:247], v[26:27], v[248:249]
	v_pk_fma_f32 v[250:251], v[246:247], v[58:59], v[250:251]
	ds_read_b128 v[244:247], v129
	s_waitcnt lgkmcnt(6)
	v_pk_fma_f32 v[248:249], v[214:215], v[24:25], v[248:249]
	v_pk_fma_f32 v[250:251], v[214:215], v[56:57], v[250:251]
	v_pk_fma_f32 v[248:249], v[216:217], v[22:23], v[248:249]
	v_pk_fma_f32 v[250:251], v[216:217], v[54:55], v[250:251]
	ds_read_b128 v[214:217], v130
	s_waitcnt lgkmcnt(6)
	v_pk_fma_f32 v[248:249], v[224:225], v[20:21], v[248:249]
	v_pk_fma_f32 v[250:251], v[224:225], v[52:53], v[250:251]
	v_pk_fma_f32 v[248:249], v[226:227], v[18:19], v[248:249]
	v_pk_fma_f32 v[250:251], v[226:227], v[50:51], v[250:251]
	ds_read_b128 v[224:227], v131
	v_add_f32_e32 v4, v248, v249
	v_add_f32_e32 v5, v250, v251
	s_waitcnt lgkmcnt(6)
	v_pk_mul_f32 v[248:249], v[228:229], v[48:49]
	v_pk_mul_f32 v[250:251], v[228:229], v[72:73]
	v_pk_fma_f32 v[248:249], v[230:231], v[46:47], v[248:249]
	v_pk_fma_f32 v[250:251], v[230:231], v[70:71], v[250:251]
	ds_read_b128 v[228:231], v132
	s_waitcnt lgkmcnt(6)
	v_pk_fma_f32 v[248:249], v[232:233], v[44:45], v[248:249]
	v_pk_fma_f32 v[250:251], v[232:233], v[80:81], v[250:251]
	v_pk_fma_f32 v[248:249], v[234:235], v[42:43], v[248:249]
	v_pk_fma_f32 v[250:251], v[234:235], v[78:79], v[250:251]
	ds_read_b128 v[232:235], v133
	s_waitcnt lgkmcnt(6)
	v_pk_fma_f32 v[248:249], v[236:237], v[40:41], v[248:249]
	v_pk_fma_f32 v[250:251], v[236:237], v[76:77], v[250:251]
	v_pk_fma_f32 v[248:249], v[238:239], v[38:39], v[248:249]
	v_pk_fma_f32 v[250:251], v[238:239], v[74:75], v[250:251]
	ds_read_b128 v[236:239], v134
	s_waitcnt lgkmcnt(6)
	v_pk_fma_f32 v[248:249], v[240:241], v[32:33], v[248:249]
	v_pk_fma_f32 v[250:251], v[240:241], v[64:65], v[250:251]
	v_pk_fma_f32 v[248:249], v[242:243], v[30:31], v[248:249]
	v_pk_fma_f32 v[250:251], v[242:243], v[62:63], v[250:251]
	ds_read_b128 v[240:243], v135
	s_waitcnt lgkmcnt(6)
	v_pk_fma_f32 v[248:249], v[244:245], v[36:37], v[248:249]
	v_pk_fma_f32 v[250:251], v[244:245], v[68:69], v[250:251]
	v_pk_fma_f32 v[248:249], v[246:247], v[34:35], v[248:249]
	v_pk_fma_f32 v[250:251], v[246:247], v[66:67], v[250:251]
	ds_read_b128 v[244:247], v136
	s_waitcnt lgkmcnt(6)
	v_pk_fma_f32 v[248:249], v[214:215], v[28:29], v[248:249]
	v_pk_fma_f32 v[250:251], v[214:215], v[60:61], v[250:251]
	v_pk_fma_f32 v[248:249], v[216:217], v[26:27], v[248:249]
	v_pk_fma_f32 v[250:251], v[216:217], v[58:59], v[250:251]
	ds_read_b128 v[214:217], v137
	s_waitcnt lgkmcnt(6)
	v_pk_fma_f32 v[248:249], v[224:225], v[24:25], v[248:249]
	v_pk_fma_f32 v[250:251], v[224:225], v[56:57], v[250:251]
	v_pk_fma_f32 v[248:249], v[226:227], v[22:23], v[248:249]
	v_pk_fma_f32 v[250:251], v[226:227], v[54:55], v[250:251]
	ds_read_b128 v[224:227], v138
	s_waitcnt lgkmcnt(6)
	v_pk_fma_f32 v[248:249], v[228:229], v[20:21], v[248:249]
	v_pk_fma_f32 v[250:251], v[228:229], v[52:53], v[250:251]
	v_pk_fma_f32 v[248:249], v[230:231], v[18:19], v[248:249]
	v_pk_fma_f32 v[250:251], v[230:231], v[50:51], v[250:251]
	ds_read_b128 v[228:231], v139
	v_add_f32_e32 v6, v248, v249
	v_add_f32_e32 v7, v250, v251
	s_waitcnt lgkmcnt(6)
	v_pk_mul_f32 v[248:249], v[232:233], v[48:49]
	v_pk_mul_f32 v[250:251], v[232:233], v[72:73]
	v_pk_fma_f32 v[248:249], v[234:235], v[46:47], v[248:249]
	v_pk_fma_f32 v[250:251], v[234:235], v[70:71], v[250:251]
	ds_read_b128 v[232:235], v140
	s_waitcnt lgkmcnt(6)
	v_pk_fma_f32 v[248:249], v[236:237], v[44:45], v[248:249]
	v_pk_fma_f32 v[250:251], v[236:237], v[80:81], v[250:251]
	v_pk_fma_f32 v[248:249], v[238:239], v[42:43], v[248:249]
	v_pk_fma_f32 v[250:251], v[238:239], v[78:79], v[250:251]
	ds_read_b128 v[236:239], v141
	s_waitcnt lgkmcnt(6)
	v_pk_fma_f32 v[248:249], v[240:241], v[40:41], v[248:249]
	v_pk_fma_f32 v[250:251], v[240:241], v[76:77], v[250:251]
	v_pk_fma_f32 v[248:249], v[242:243], v[38:39], v[248:249]
	v_pk_fma_f32 v[250:251], v[242:243], v[74:75], v[250:251]
	ds_read_b128 v[240:243], v142
	s_waitcnt lgkmcnt(6)
	v_pk_fma_f32 v[248:249], v[244:245], v[32:33], v[248:249]
	v_pk_fma_f32 v[250:251], v[244:245], v[64:65], v[250:251]
	v_pk_fma_f32 v[248:249], v[246:247], v[30:31], v[248:249]
	v_pk_fma_f32 v[250:251], v[246:247], v[62:63], v[250:251]
	ds_read_b128 v[244:247], v143
	s_waitcnt lgkmcnt(6)
	v_pk_fma_f32 v[248:249], v[214:215], v[36:37], v[248:249]
	v_pk_fma_f32 v[250:251], v[214:215], v[68:69], v[250:251]
	v_pk_fma_f32 v[248:249], v[216:217], v[34:35], v[248:249]
	v_pk_fma_f32 v[250:251], v[216:217], v[66:67], v[250:251]
	ds_read_b128 v[214:217], v144
	s_waitcnt lgkmcnt(6)
	v_pk_fma_f32 v[248:249], v[224:225], v[28:29], v[248:249]
	v_pk_fma_f32 v[250:251], v[224:225], v[60:61], v[250:251]
	v_pk_fma_f32 v[248:249], v[226:227], v[26:27], v[248:249]
	v_pk_fma_f32 v[250:251], v[226:227], v[58:59], v[250:251]
	ds_read_b128 v[224:227], v145
	s_waitcnt lgkmcnt(6)
	v_pk_fma_f32 v[248:249], v[228:229], v[24:25], v[248:249]
	v_pk_fma_f32 v[250:251], v[228:229], v[56:57], v[250:251]
	v_pk_fma_f32 v[248:249], v[230:231], v[22:23], v[248:249]
	v_pk_fma_f32 v[250:251], v[230:231], v[54:55], v[250:251]
	ds_read_b128 v[228:231], v146
	s_waitcnt lgkmcnt(6)
	v_pk_fma_f32 v[248:249], v[232:233], v[20:21], v[248:249]
	v_pk_fma_f32 v[250:251], v[232:233], v[52:53], v[250:251]
	v_pk_fma_f32 v[248:249], v[234:235], v[18:19], v[248:249]
	v_pk_fma_f32 v[250:251], v[234:235], v[50:51], v[250:251]
	ds_read_b128 v[232:235], v147
	v_add_f32_e32 v97, v248, v249
	v_add_f32_e32 v98, v250, v251
	s_waitcnt lgkmcnt(6)
	v_pk_mul_f32 v[248:249], v[236:237], v[48:49]
	v_pk_mul_f32 v[250:251], v[236:237], v[72:73]
	v_pk_fma_f32 v[248:249], v[238:239], v[46:47], v[248:249]
	v_pk_fma_f32 v[250:251], v[238:239], v[70:71], v[250:251]
	ds_read_b128 v[236:239], v148
	s_waitcnt lgkmcnt(6)
	v_pk_fma_f32 v[248:249], v[240:241], v[44:45], v[248:249]
	v_pk_fma_f32 v[250:251], v[240:241], v[80:81], v[250:251]
	v_pk_fma_f32 v[248:249], v[242:243], v[42:43], v[248:249]
	v_pk_fma_f32 v[250:251], v[242:243], v[78:79], v[250:251]
	ds_read_b128 v[240:243], v149
	s_waitcnt lgkmcnt(6)
	v_pk_fma_f32 v[248:249], v[244:245], v[40:41], v[248:249]
	v_pk_fma_f32 v[250:251], v[244:245], v[76:77], v[250:251]
	v_pk_fma_f32 v[248:249], v[246:247], v[38:39], v[248:249]
	v_pk_fma_f32 v[250:251], v[246:247], v[74:75], v[250:251]
	ds_read_b128 v[244:247], v150
	s_waitcnt lgkmcnt(6)
	v_pk_fma_f32 v[248:249], v[214:215], v[32:33], v[248:249]
	v_pk_fma_f32 v[250:251], v[214:215], v[64:65], v[250:251]
	v_pk_fma_f32 v[248:249], v[216:217], v[30:31], v[248:249]
	v_pk_fma_f32 v[250:251], v[216:217], v[62:63], v[250:251]
	ds_read_b128 v[214:217], v151
	s_waitcnt lgkmcnt(6)
	v_pk_fma_f32 v[248:249], v[224:225], v[36:37], v[248:249]
	v_pk_fma_f32 v[250:251], v[224:225], v[68:69], v[250:251]
	v_pk_fma_f32 v[248:249], v[226:227], v[34:35], v[248:249]
	v_pk_fma_f32 v[250:251], v[226:227], v[66:67], v[250:251]
	ds_read_b128 v[224:227], v152
	s_waitcnt lgkmcnt(6)
	v_pk_fma_f32 v[248:249], v[228:229], v[28:29], v[248:249]
	v_pk_fma_f32 v[250:251], v[228:229], v[60:61], v[250:251]
	v_pk_fma_f32 v[248:249], v[230:231], v[26:27], v[248:249]
	v_pk_fma_f32 v[250:251], v[230:231], v[58:59], v[250:251]
	ds_read_b128 v[228:231], v153
	s_waitcnt lgkmcnt(6)
	v_pk_fma_f32 v[248:249], v[232:233], v[24:25], v[248:249]
	v_pk_fma_f32 v[250:251], v[232:233], v[56:57], v[250:251]
	v_pk_fma_f32 v[248:249], v[234:235], v[22:23], v[248:249]
	v_pk_fma_f32 v[250:251], v[234:235], v[54:55], v[250:251]
	ds_read_b128 v[232:235], v154
	s_waitcnt lgkmcnt(6)
	v_pk_fma_f32 v[248:249], v[236:237], v[20:21], v[248:249]
	v_pk_fma_f32 v[250:251], v[236:237], v[52:53], v[250:251]
	v_pk_fma_f32 v[248:249], v[238:239], v[18:19], v[248:249]
	v_pk_fma_f32 v[250:251], v[238:239], v[50:51], v[250:251]
	ds_read_b128 v[236:239], v155
	v_add_f32_e32 v99, v248, v249
	v_add_f32_e32 v100, v250, v251
	s_waitcnt lgkmcnt(6)
	v_pk_mul_f32 v[248:249], v[240:241], v[48:49]
	v_pk_mul_f32 v[250:251], v[240:241], v[72:73]
	v_pk_fma_f32 v[248:249], v[242:243], v[46:47], v[248:249]
	v_pk_fma_f32 v[250:251], v[242:243], v[70:71], v[250:251]
	ds_read_b128 v[240:243], v156
	s_waitcnt lgkmcnt(6)
	v_pk_fma_f32 v[248:249], v[244:245], v[44:45], v[248:249]
	v_pk_fma_f32 v[250:251], v[244:245], v[80:81], v[250:251]
	v_pk_fma_f32 v[248:249], v[246:247], v[42:43], v[248:249]
	v_pk_fma_f32 v[250:251], v[246:247], v[78:79], v[250:251]
	ds_read_b128 v[244:247], v157
	s_waitcnt lgkmcnt(6)
	v_pk_fma_f32 v[248:249], v[214:215], v[40:41], v[248:249]
	v_pk_fma_f32 v[250:251], v[214:215], v[76:77], v[250:251]
	v_pk_fma_f32 v[248:249], v[216:217], v[38:39], v[248:249]
	v_pk_fma_f32 v[250:251], v[216:217], v[74:75], v[250:251]
	ds_read_b128 v[214:217], v158
	s_waitcnt lgkmcnt(6)
	v_pk_fma_f32 v[248:249], v[224:225], v[32:33], v[248:249]
	v_pk_fma_f32 v[250:251], v[224:225], v[64:65], v[250:251]
	v_pk_fma_f32 v[248:249], v[226:227], v[30:31], v[248:249]
	v_pk_fma_f32 v[250:251], v[226:227], v[62:63], v[250:251]
	ds_read_b128 v[224:227], v159
	s_waitcnt lgkmcnt(6)
	v_pk_fma_f32 v[248:249], v[228:229], v[36:37], v[248:249]
	v_pk_fma_f32 v[250:251], v[228:229], v[68:69], v[250:251]
	v_pk_fma_f32 v[248:249], v[230:231], v[34:35], v[248:249]
	v_pk_fma_f32 v[250:251], v[230:231], v[66:67], v[250:251]
	ds_read_b128 v[228:231], v160
	s_waitcnt lgkmcnt(6)
	v_pk_fma_f32 v[248:249], v[232:233], v[28:29], v[248:249]
	v_pk_fma_f32 v[250:251], v[232:233], v[60:61], v[250:251]
	v_pk_fma_f32 v[248:249], v[234:235], v[26:27], v[248:249]
	v_pk_fma_f32 v[250:251], v[234:235], v[58:59], v[250:251]
	ds_read_b128 v[232:235], v161
	s_waitcnt lgkmcnt(6)
	v_pk_fma_f32 v[248:249], v[236:237], v[24:25], v[248:249]
	v_pk_fma_f32 v[250:251], v[236:237], v[56:57], v[250:251]
	v_pk_fma_f32 v[248:249], v[238:239], v[22:23], v[248:249]
	v_pk_fma_f32 v[250:251], v[238:239], v[54:55], v[250:251]
	ds_read_b128 v[236:239], v162
	s_waitcnt lgkmcnt(6)
	v_pk_fma_f32 v[248:249], v[240:241], v[20:21], v[248:249]
	v_pk_fma_f32 v[250:251], v[240:241], v[52:53], v[250:251]
	v_pk_fma_f32 v[248:249], v[242:243], v[18:19], v[248:249]
	v_pk_fma_f32 v[250:251], v[242:243], v[50:51], v[250:251]
	ds_read_b128 v[240:243], v163
	v_add_f32_e32 v101, v248, v249
	v_add_f32_e32 v102, v250, v251
	s_waitcnt lgkmcnt(6)
	v_pk_mul_f32 v[248:249], v[244:245], v[48:49]
	v_pk_mul_f32 v[250:251], v[244:245], v[72:73]
	v_pk_fma_f32 v[248:249], v[246:247], v[46:47], v[248:249]
	v_pk_fma_f32 v[250:251], v[246:247], v[70:71], v[250:251]
	ds_read_b128 v[244:247], v164
	s_waitcnt lgkmcnt(6)
	v_pk_fma_f32 v[248:249], v[214:215], v[44:45], v[248:249]
	v_pk_fma_f32 v[250:251], v[214:215], v[80:81], v[250:251]
	v_pk_fma_f32 v[248:249], v[216:217], v[42:43], v[248:249]
	v_pk_fma_f32 v[250:251], v[216:217], v[78:79], v[250:251]
	s_waitcnt lgkmcnt(5)
	v_pk_fma_f32 v[248:249], v[224:225], v[40:41], v[248:249]
	v_pk_fma_f32 v[250:251], v[224:225], v[76:77], v[250:251]
	v_pk_fma_f32 v[248:249], v[226:227], v[38:39], v[248:249]
	v_pk_fma_f32 v[250:251], v[226:227], v[74:75], v[250:251]
	s_waitcnt lgkmcnt(4)
	v_pk_fma_f32 v[248:249], v[228:229], v[32:33], v[248:249]
	v_pk_fma_f32 v[250:251], v[228:229], v[64:65], v[250:251]
	v_pk_fma_f32 v[248:249], v[230:231], v[30:31], v[248:249]
	v_pk_fma_f32 v[250:251], v[230:231], v[62:63], v[250:251]
	s_waitcnt lgkmcnt(3)
	v_pk_fma_f32 v[248:249], v[232:233], v[36:37], v[248:249]
	v_pk_fma_f32 v[250:251], v[232:233], v[68:69], v[250:251]
	v_pk_fma_f32 v[248:249], v[234:235], v[34:35], v[248:249]
	v_pk_fma_f32 v[250:251], v[234:235], v[66:67], v[250:251]
	s_waitcnt lgkmcnt(2)
	v_pk_fma_f32 v[248:249], v[236:237], v[28:29], v[248:249]
	v_pk_fma_f32 v[250:251], v[236:237], v[60:61], v[250:251]
	v_pk_fma_f32 v[248:249], v[238:239], v[26:27], v[248:249]
	v_pk_fma_f32 v[250:251], v[238:239], v[58:59], v[250:251]
	s_waitcnt lgkmcnt(1)
	v_pk_fma_f32 v[248:249], v[240:241], v[24:25], v[248:249]
	v_pk_fma_f32 v[250:251], v[240:241], v[56:57], v[250:251]
	v_pk_fma_f32 v[248:249], v[242:243], v[22:23], v[248:249]
	v_pk_fma_f32 v[250:251], v[242:243], v[54:55], v[250:251]
	s_waitcnt lgkmcnt(0)
	v_pk_fma_f32 v[248:249], v[244:245], v[20:21], v[248:249]
	v_pk_fma_f32 v[250:251], v[244:245], v[52:53], v[250:251]
	v_pk_fma_f32 v[248:249], v[246:247], v[18:19], v[248:249]
	v_pk_fma_f32 v[250:251], v[246:247], v[50:51], v[250:251]
	v_add_f32_e32 v103, v248, v249
	v_add_f32_e32 v104, v250, v251
	ds_read_b128 v[224:227], v165
	ds_read_b128 v[106:109], v166
	ds_read_b128 v[240:243], v167
	ds_read_b128 v[236:239], v168
	ds_read_b128 v[232:235], v169
	ds_read_b128 v[228:231], v170
	s_waitcnt lgkmcnt(5)
	v_mul_f32_e32 v105, v225, v49
	v_mul_f32_e32 v225, v225, v73
	v_fmac_f32_e32 v105, v224, v48
	v_fmac_f32_e32 v225, v224, v72
	v_mul_f32_e32 v224, v227, v71
	v_mul_f32_e32 v191, v227, v47
	v_fmac_f32_e32 v224, v226, v70
	v_fmac_f32_e32 v191, v226, v46
	v_add_f32_e32 v224, v225, v224
	v_add_f32_e32 v105, v105, v191
	v_add_f32_e32 v191, 0, v224
	ds_read_b128 v[224:227], v171
	v_add_f32_e32 v105, 0, v105
	s_waitcnt lgkmcnt(5)
	v_mul_f32_e32 v192, v107, v45
	v_mul_f32_e32 v107, v107, v81
	v_fmac_f32_e32 v192, v106, v44
	v_fmac_f32_e32 v107, v106, v80
	v_mul_f32_e32 v106, v109, v79
	v_fmac_f32_e32 v106, v108, v78
	v_mul_f32_e32 v193, v109, v43
	v_add_f32_e32 v106, v107, v106
	v_fmac_f32_e32 v193, v108, v42
	v_add_f32_e32 v191, v191, v106
	ds_read_b128 v[106:109], v172
	v_add_f32_e32 v192, v192, v193
	v_add_f32_e32 v105, v105, v192
	s_waitcnt lgkmcnt(5)
	v_mul_f32_e32 v192, v241, v41
	v_mul_f32_e32 v241, v241, v77
	v_fmac_f32_e32 v192, v240, v40
	v_fmac_f32_e32 v241, v240, v76
	v_mul_f32_e32 v240, v243, v75
	v_fmac_f32_e32 v240, v242, v74
	v_mul_f32_e32 v193, v243, v39
	v_add_f32_e32 v240, v241, v240
	v_fmac_f32_e32 v193, v242, v38
	v_add_f32_e32 v191, v191, v240
	v_add_f32_e32 v192, v192, v193
	v_add_f32_e32 v105, v105, v192
	s_waitcnt lgkmcnt(4)
	v_mul_f32_e32 v192, v237, v33
	v_mul_f32_e32 v237, v237, v65
	v_fmac_f32_e32 v192, v236, v32
	v_fmac_f32_e32 v237, v236, v64
	v_mul_f32_e32 v236, v239, v63
	v_fmac_f32_e32 v236, v238, v62
	v_mul_f32_e32 v193, v239, v31
	v_add_f32_e32 v236, v237, v236
	v_fmac_f32_e32 v193, v238, v30
	v_add_f32_e32 v191, v191, v236
	v_add_f32_e32 v192, v192, v193
	v_add_f32_e32 v105, v105, v192
	s_waitcnt lgkmcnt(3)
	v_mul_f32_e32 v192, v233, v37
	v_mul_f32_e32 v233, v233, v69
	v_fmac_f32_e32 v192, v232, v36
	v_fmac_f32_e32 v233, v232, v68
	v_mul_f32_e32 v232, v235, v67
	v_fmac_f32_e32 v232, v234, v66
	v_mul_f32_e32 v193, v235, v35
	v_add_f32_e32 v232, v233, v232
	v_fmac_f32_e32 v193, v234, v34
	v_add_f32_e32 v191, v191, v232
	v_add_f32_e32 v192, v192, v193
	v_add_f32_e32 v105, v105, v192
	s_waitcnt lgkmcnt(2)
	v_mul_f32_e32 v192, v229, v29
	v_mul_f32_e32 v229, v229, v61
	v_fmac_f32_e32 v192, v228, v28
	v_fmac_f32_e32 v229, v228, v60
	v_mul_f32_e32 v228, v231, v59
	v_fmac_f32_e32 v228, v230, v58
	v_mul_f32_e32 v193, v231, v27
	v_add_f32_e32 v228, v229, v228
	v_fmac_f32_e32 v193, v230, v26
	v_add_f32_e32 v191, v191, v228
	v_add_f32_e32 v192, v192, v193
	v_add_f32_e32 v105, v105, v192
	s_waitcnt lgkmcnt(1)
	v_mul_f32_e32 v192, v225, v25
	v_mul_f32_e32 v225, v225, v57
	v_fmac_f32_e32 v192, v224, v24
	v_fmac_f32_e32 v225, v224, v56
	v_mul_f32_e32 v224, v227, v55
	v_fmac_f32_e32 v224, v226, v54
	v_mul_f32_e32 v193, v227, v23
	v_add_f32_e32 v224, v225, v224
	v_fmac_f32_e32 v193, v226, v22
	v_add_f32_e32 v191, v191, v224
	v_add_f32_e32 v192, v192, v193
	v_add_f32_e32 v105, v105, v192
	s_waitcnt lgkmcnt(0)
	v_mul_f32_e32 v192, v107, v21
	v_mul_f32_e32 v193, v109, v19
	v_fmac_f32_e32 v192, v106, v20
	v_fmac_f32_e32 v193, v108, v18
	v_add_f32_e32 v192, v192, v193
	v_add_f32_e32 v105, v105, v192
	ds_read_b128 v[192:195], v173
	v_mul_f32_e32 v107, v107, v53
	v_fmac_f32_e32 v107, v106, v52
	v_mul_f32_e32 v106, v109, v51
	v_fmac_f32_e32 v106, v108, v50
	s_waitcnt lgkmcnt(0)
	v_mul_f32_e32 v49, v193, v49
	v_mul_f32_e32 v47, v195, v47
	v_fmac_f32_e32 v49, v192, v48
	v_fmac_f32_e32 v47, v194, v46
	v_add_f32_e32 v46, v49, v47
	v_add_f32_e32 v106, v107, v106
	v_add_f32_e32 v107, 0, v46
	v_mul_f32_e32 v46, v193, v73
	v_mul_f32_e32 v47, v195, v71
	v_fmac_f32_e32 v46, v192, v72
	v_fmac_f32_e32 v47, v194, v70
	v_add_f32_e32 v46, v46, v47
	v_add_f32_e32 v70, 0, v46
	ds_read_b128 v[46:49], v174
	v_add_f32_e32 v106, v191, v106
	s_waitcnt lgkmcnt(0)
	v_mul_f32_e32 v45, v47, v45
	v_mul_f32_e32 v43, v49, v43
	v_fmac_f32_e32 v45, v46, v44
	v_fmac_f32_e32 v43, v48, v42
	v_add_f32_e32 v42, v45, v43
	v_add_f32_e32 v71, v107, v42
	v_mul_f32_e32 v42, v47, v81
	v_mul_f32_e32 v43, v49, v79
	v_fmac_f32_e32 v42, v46, v80
	v_fmac_f32_e32 v43, v48, v78
	v_add_f32_e32 v42, v42, v43
	v_add_f32_e32 v46, v70, v42
	ds_read_b128 v[42:45], v175
	s_waitcnt lgkmcnt(0)
	v_mul_f32_e32 v41, v43, v41
	v_mul_f32_e32 v39, v45, v39
	v_fmac_f32_e32 v41, v42, v40
	v_fmac_f32_e32 v39, v44, v38
	v_add_f32_e32 v38, v41, v39
	v_add_f32_e32 v47, v71, v38
	v_mul_f32_e32 v38, v43, v77
	v_mul_f32_e32 v39, v45, v75
	v_fmac_f32_e32 v38, v42, v76
	v_fmac_f32_e32 v39, v44, v74
	v_add_f32_e32 v38, v38, v39
	v_add_f32_e32 v42, v46, v38
	ds_read_b128 v[38:41], v176
	s_waitcnt lgkmcnt(0)
	v_mul_f32_e32 v33, v39, v33
	v_mul_f32_e32 v31, v41, v31
	v_fmac_f32_e32 v33, v38, v32
	v_fmac_f32_e32 v31, v40, v30
	v_add_f32_e32 v30, v33, v31
	v_add_f32_e32 v43, v47, v30
	v_mul_f32_e32 v30, v39, v65
	v_mul_f32_e32 v31, v41, v63
	v_fmac_f32_e32 v30, v38, v64
	v_fmac_f32_e32 v31, v40, v62
	v_add_f32_e32 v30, v30, v31
	v_add_f32_e32 v38, v42, v30
	ds_read_b128 v[224:227], v177
	ds_read_b128 v[30:33], v178
	s_waitcnt lgkmcnt(1)
	v_mul_f32_e32 v37, v225, v37
	v_mul_f32_e32 v225, v225, v69
	v_fmac_f32_e32 v37, v224, v36
	v_fmac_f32_e32 v225, v224, v68
	v_mul_f32_e32 v224, v227, v67
	v_mul_f32_e32 v35, v227, v35
	v_fmac_f32_e32 v224, v226, v66
	v_fmac_f32_e32 v35, v226, v34
	v_add_f32_e32 v224, v225, v224
	v_add_f32_e32 v34, v37, v35
	v_add_f32_e32 v35, v38, v224
	v_add_f32_e32 v34, v43, v34
	s_waitcnt lgkmcnt(0)
	v_mul_f32_e32 v29, v31, v29
	v_mul_f32_e32 v27, v33, v27
	v_fmac_f32_e32 v29, v30, v28
	v_fmac_f32_e32 v27, v32, v26
	v_add_f32_e32 v26, v29, v27
	v_add_f32_e32 v34, v34, v26
	v_mul_f32_e32 v26, v31, v61
	v_mul_f32_e32 v27, v33, v59
	v_fmac_f32_e32 v26, v30, v60
	v_fmac_f32_e32 v27, v32, v58
	v_add_f32_e32 v26, v26, v27
	v_add_f32_e32 v30, v35, v26
	ds_read_b128 v[26:29], v179
	s_waitcnt lgkmcnt(0)
	v_mul_f32_e32 v25, v27, v25
	v_mul_f32_e32 v23, v29, v23
	v_fmac_f32_e32 v25, v26, v24
	v_fmac_f32_e32 v23, v28, v22
	v_add_f32_e32 v22, v25, v23
	v_add_f32_e32 v31, v34, v22
	v_mul_f32_e32 v22, v27, v57
	v_mul_f32_e32 v23, v29, v55
	v_fmac_f32_e32 v22, v26, v56
	v_fmac_f32_e32 v23, v28, v54
	v_add_f32_e32 v22, v22, v23
	v_add_f32_e32 v26, v30, v22
	ds_read_b128 v[22:25], v180
	v_cndmask_b32_e64 v27, v92, v104, s[34:35]
	v_cndmask_b32_e64 v28, v104, v92, s[34:35]
	v_cndmask_b32_e64 v29, v94, v106, s[34:35]
	v_cndmask_b32_e64 v30, v106, v94, s[34:35]
	s_waitcnt lgkmcnt(0)
	v_mul_f32_e32 v21, v23, v21
	v_mul_f32_e32 v19, v25, v19
	v_fmac_f32_e32 v21, v22, v20
	v_fmac_f32_e32 v19, v24, v18
	v_add_f32_e32 v18, v21, v19
	v_mul_f32_e32 v19, v23, v53
	v_mul_f32_e32 v20, v25, v51
	v_fmac_f32_e32 v19, v22, v52
	v_fmac_f32_e32 v20, v24, v50
	v_add_f32_e32 v19, v19, v20
	v_cndmask_b32_e64 v20, v2, v4, s[34:35]
	v_cndmask_b32_e64 v2, v4, v2, s[34:35]
	v_cndmask_b32_e64 v4, v82, v5, s[34:35]
	ds_bpermute_b32 v4, v112, v4
	v_cndmask_b32_e64 v5, v5, v82, s[34:35]
	ds_bpermute_b32 v20, v112, v20
	v_cndmask_b32_e64 v21, v86, v98, s[34:35]
	v_cndmask_b32_e64 v22, v98, v86, s[34:35]
	s_waitcnt lgkmcnt(1)
	v_add_f32_e32 v4, v5, v4
	v_cndmask_b32_e64 v5, v83, v6, s[34:35]
	ds_bpermute_b32 v5, v112, v5
	s_waitcnt lgkmcnt(1)
	v_add_f32_e32 v2, v2, v20
	v_cndmask_b32_e64 v6, v6, v83, s[34:35]
	v_cndmask_b32_e64 v20, v84, v7, s[34:35]
	v_cndmask_b32_e64 v7, v7, v84, s[34:35]
	s_waitcnt lgkmcnt(0)
	v_add_f32_e32 v5, v6, v5
	ds_bpermute_b32 v6, v112, v20
	v_cndmask_b32_e64 v20, v97, v85, s[34:35]
	v_cndmask_b32_e64 v23, v88, v100, s[34:35]
	v_cndmask_b32_e64 v24, v100, v88, s[34:35]
	v_cndmask_b32_e64 v25, v90, v102, s[34:35]
	s_waitcnt lgkmcnt(0)
	v_add_f32_e32 v6, v7, v6
	v_cndmask_b32_e64 v7, v85, v97, s[34:35]
	ds_bpermute_b32 v7, v112, v7
	v_add_f32_e32 v19, v26, v19
	v_cndmask_b32_e64 v26, v102, v90, s[34:35]
	v_add_f32_e32 v18, v31, v18
	s_waitcnt lgkmcnt(0)
	v_add_f32_e32 v7, v20, v7
	ds_bpermute_b32 v20, v112, v21
	v_cndmask_b32_e64 v21, v87, v99, s[34:35]
	ds_bpermute_b32 v21, v112, v21
	s_waitcnt lgkmcnt(1)
	v_add_f32_e32 v20, v22, v20
	v_cndmask_b32_e64 v22, v99, v87, s[34:35]
	s_waitcnt lgkmcnt(0)
	v_add_f32_e32 v21, v22, v21
	ds_bpermute_b32 v22, v112, v23
	v_cndmask_b32_e64 v23, v89, v101, s[34:35]
	ds_bpermute_b32 v23, v112, v23
	s_waitcnt lgkmcnt(1)
	v_add_f32_e32 v22, v24, v22
	v_cndmask_b32_e64 v24, v101, v89, s[34:35]
	s_waitcnt lgkmcnt(0)
	v_add_f32_e32 v23, v24, v23
	ds_bpermute_b32 v24, v112, v25
	v_cndmask_b32_e64 v25, v91, v103, s[34:35]
	ds_bpermute_b32 v25, v112, v25
	s_waitcnt lgkmcnt(1)
	v_add_f32_e32 v24, v26, v24
	v_cndmask_b32_e64 v26, v103, v91, s[34:35]
	s_waitcnt lgkmcnt(0)
	v_add_f32_e32 v25, v26, v25
	ds_bpermute_b32 v26, v112, v27
	v_cndmask_b32_e64 v27, v93, v105, s[34:35]
	ds_bpermute_b32 v27, v112, v27
	s_waitcnt lgkmcnt(1)
	v_add_f32_e32 v26, v28, v26
	v_cndmask_b32_e64 v28, v105, v93, s[34:35]
	s_waitcnt lgkmcnt(0)
	v_add_f32_e32 v27, v28, v27
	ds_bpermute_b32 v28, v112, v29
	v_cndmask_b32_e64 v29, v95, v18, s[34:35]
	ds_bpermute_b32 v29, v112, v29
	v_cndmask_b32_e64 v18, v18, v95, s[34:35]
	s_waitcnt lgkmcnt(1)
	v_add_f32_e32 v28, v30, v28
	v_cndmask_b32_e64 v30, v96, v19, s[34:35]
	s_waitcnt lgkmcnt(0)
	v_add_f32_e32 v18, v18, v29
	ds_bpermute_b32 v29, v112, v30
	v_cndmask_b32_e64 v19, v19, v96, s[34:35]
	s_waitcnt lgkmcnt(0)
	v_add_f32_e32 v19, v19, v29
	v_cndmask_b32_e64 v29, v2, v23, s[36:37]
	v_cndmask_b32_e64 v2, v23, v2, s[36:37]
	v_cndmask_b32_e64 v23, v4, v24, s[36:37]
	ds_bpermute_b32 v23, v111, v23
	v_cndmask_b32_e64 v4, v24, v4, s[36:37]
	ds_bpermute_b32 v24, v111, v29
	s_waitcnt lgkmcnt(1)
	v_add_f32_e32 v4, v4, v23
	v_cndmask_b32_e64 v23, v5, v25, s[36:37]
	ds_bpermute_b32 v23, v111, v23
	s_waitcnt lgkmcnt(1)
	v_add_f32_e32 v2, v2, v24
	v_cndmask_b32_e64 v5, v25, v5, s[36:37]
	v_cndmask_b32_e64 v24, v6, v26, s[36:37]
	v_cndmask_b32_e64 v6, v26, v6, s[36:37]
	s_waitcnt lgkmcnt(0)
	v_add_f32_e32 v5, v5, v23
	ds_bpermute_b32 v23, v111, v24
	v_cndmask_b32_e64 v24, v20, v28, s[36:37]
	v_cndmask_b32_e64 v20, v28, v20, s[36:37]
	s_waitcnt lgkmcnt(0)
	v_add_f32_e32 v6, v6, v23
	v_cndmask_b32_e64 v23, v7, v27, s[36:37]
	ds_bpermute_b32 v23, v111, v23
	v_cndmask_b32_e64 v7, v27, v7, s[36:37]
	s_waitcnt lgkmcnt(0)
	v_add_f32_e32 v7, v7, v23
	ds_bpermute_b32 v23, v111, v24
	s_waitcnt lgkmcnt(0)
	v_add_f32_e32 v20, v20, v23
	v_cndmask_b32_e64 v23, v21, v18, s[36:37]
	v_cndmask_b32_e64 v18, v18, v21, s[36:37]
	v_cndmask_b32_e64 v21, v22, v19, s[36:37]
	ds_bpermute_b32 v21, v111, v21
	v_cndmask_b32_e64 v19, v19, v22, s[36:37]
	ds_bpermute_b32 v22, v111, v23
	s_waitcnt lgkmcnt(1)
	v_add_f32_e32 v19, v19, v21
	v_cndmask_b32_e64 v21, v2, v7, s[38:39]
	v_cndmask_b32_e64 v2, v7, v2, s[38:39]
	v_cndmask_b32_e64 v7, v4, v20, s[38:39]
	ds_bpermute_b32 v7, v113, v7
	s_waitcnt lgkmcnt(1)
	v_add_f32_e32 v18, v18, v22
	v_cndmask_b32_e64 v4, v20, v4, s[38:39]
	ds_bpermute_b32 v20, v113, v21
	s_waitcnt lgkmcnt(1)
	v_add_f32_e32 v4, v4, v7
	v_cndmask_b32_e64 v7, v5, v18, s[38:39]
	ds_bpermute_b32 v7, v113, v7
	v_cndmask_b32_e64 v5, v18, v5, s[38:39]
	v_cndmask_b32_e64 v18, v6, v19, s[38:39]
	s_waitcnt lgkmcnt(1)
	v_add_f32_e32 v2, v2, v20
	v_cndmask_b32_e64 v6, v19, v6, s[38:39]
	s_waitcnt lgkmcnt(0)
	v_add_f32_e32 v5, v5, v7
	ds_bpermute_b32 v7, v113, v18
	s_waitcnt lgkmcnt(0)
	v_add_f32_e32 v6, v6, v7
	v_cndmask_b32_e64 v7, v2, v5, s[40:41]
	v_cndmask_b32_e64 v2, v5, v2, s[40:41]
	v_cndmask_b32_e64 v5, v4, v6, s[40:41]
	v_cndmask_b32_e64 v4, v6, v4, s[40:41]
	ds_bpermute_b32 v6, v114, v7
	ds_bpermute_b32 v5, v114, v5
	s_waitcnt lgkmcnt(1)
	v_add_f32_e32 v2, v2, v6
	s_waitcnt lgkmcnt(0)
	v_add_f32_e32 v4, v4, v5
	ds_bpermute_b32 v5, v115, v2
	s_waitcnt lgkmcnt(0)
	v_add_f32_e32 v2, v2, v5
	ds_bpermute_b32 v5, v115, v4
	s_waitcnt lgkmcnt(0)
	v_add_f32_e32 v4, v4, v5
	ds_bpermute_b32 v5, v116, v2
	s_waitcnt lgkmcnt(0)
	v_add_f32_e32 v2, v2, v5
	ds_bpermute_b32 v5, v116, v4
	s_waitcnt lgkmcnt(0)
	v_add_f32_e32 v5, v4, v5
	ds_bpermute_b32 v4, v114, v2
	ds_bpermute_b32 v6, v114, v5
	s_waitcnt lgkmcnt(1)
	v_max_f32_e32 v4, v4, v4
	v_max_f32_e32 v4, v2, v4
	ds_bpermute_b32 v7, v113, v4
	s_waitcnt lgkmcnt(1)
	v_max_f32_e32 v6, v6, v6
	v_max_f32_e32 v6, v5, v6
	s_waitcnt lgkmcnt(0)
	v_max_f32_e32 v7, v7, v7
	v_max_f32_e32 v4, v4, v7
	ds_bpermute_b32 v7, v113, v6
	s_waitcnt lgkmcnt(0)
	v_max_f32_e32 v7, v7, v7
	v_max_f32_e32 v6, v6, v7
	ds_bpermute_b32 v7, v111, v4
	s_waitcnt lgkmcnt(0)
	v_max_f32_e32 v7, v7, v7
	v_max_f32_e32 v4, v4, v7
	ds_bpermute_b32 v7, v111, v6
	s_waitcnt lgkmcnt(0)
	v_max_f32_e32 v7, v7, v7
	v_max_f32_e32 v6, v6, v7
	ds_bpermute_b32 v7, v112, v4
	s_waitcnt lgkmcnt(0)
	v_max_f32_e32 v7, v7, v7
	v_max_f32_e32 v4, v4, v7
	ds_bpermute_b32 v7, v112, v6
	v_sub_f32_e32 v2, v2, v4
	v_mul_f32_e32 v2, 0x3fb8aa3b, v2
	v_exp_f32_e32 v4, v2
	s_waitcnt lgkmcnt(0)
	v_max_f32_e32 v7, v7, v7
	v_max_f32_e32 v6, v6, v7
	v_sub_f32_e32 v2, v5, v6
	v_mul_f32_e32 v2, 0x3fb8aa3b, v2
	ds_bpermute_b32 v5, v114, v4
	v_exp_f32_e32 v2, v2
	s_waitcnt lgkmcnt(0)
	v_add_f32_e32 v5, v4, v5
	ds_bpermute_b32 v6, v114, v2
	ds_bpermute_b32 v7, v113, v5
	s_waitcnt lgkmcnt(1)
	v_add_f32_e32 v6, v2, v6
	s_waitcnt lgkmcnt(0)
	v_add_f32_e32 v5, v5, v7
	ds_bpermute_b32 v7, v113, v6
	s_waitcnt lgkmcnt(0)
	v_add_f32_e32 v6, v6, v7
	ds_bpermute_b32 v7, v111, v5
	s_waitcnt lgkmcnt(0)
	v_add_f32_e32 v7, v5, v7
	ds_bpermute_b32 v5, v111, v6
	ds_bpermute_b32 v18, v112, v7
	s_waitcnt lgkmcnt(1)
	v_add_f32_e32 v5, v6, v5
	ds_bpermute_b32 v6, v112, v5
	s_and_saveexec_b64 s[0:1], s[42:43]
	s_cbranch_execz .LBB0_2122
	s_waitcnt lgkmcnt(1)
	v_add_f32_e32 v7, v7, v18
	v_div_scale_f32 v18, s[2:3], v7, v7, v4
	v_rcp_f32_e32 v19, v18
	v_div_scale_f32 v20, vcc, v4, v7, v4
	s_cmp_eq_u32 s8, s48
	v_fma_f32 v21, -v18, v19, 1.0
	v_fmac_f32_e32 v19, v21, v19
	v_mul_f32_e32 v21, v20, v19
	v_fma_f32 v22, -v18, v21, v20
	v_fmac_f32_e32 v21, v22, v19
	v_fma_f32 v18, -v18, v21, v20
	v_div_fmas_f32 v18, v18, v19, v21
	v_div_fixup_f32 v4, v18, v7, v4
	v_lshl_add_u64 v[18:19], s[44:45], 0, v[14:15]
	global_store_dword v[18:19], v4, off
	s_cbranch_scc1 .LBB0_2122
	s_waitcnt lgkmcnt(0)
	v_add_f32_e32 v4, v5, v6
	v_div_scale_f32 v5, s[2:3], v4, v4, v2
	v_rcp_f32_e32 v6, v5
	v_div_scale_f32 v7, vcc, v2, v4, v2
	s_lshl_b64 s[2:3], s[48:49], 6
	v_fma_f32 v18, -v5, v6, 1.0
	v_fmac_f32_e32 v6, v18, v6
	v_mul_f32_e32 v18, v7, v6
	v_fma_f32 v19, -v5, v18, v7
	v_fmac_f32_e32 v18, v19, v6
	v_fma_f32 v5, -v5, v18, v7
	v_div_fmas_f32 v5, v5, v6, v18
	v_div_fixup_f32 v2, v5, v4, v2
	v_lshl_add_u64 v[4:5], v[10:11], 0, s[2:3]
	global_store_dword v[4:5], v2, off
	s_branch .LBB0_2122
